# nt cache hint on once-read f32 weight loads (P1/N2/N2M conversion) and on the final output stores
# speedup vs baseline: 1.0170x; 1.0170x over previous
.LBB0_20:
	s_cmpk_gt_i32 s11, 0x64f
	s_mov_b64 s[2:3], -1
	s_cbranch_scc0 .LBB0_42
	s_cmpk_gt_u32 s11, 0xe4f
	s_cbranch_scc0 .LBB0_39
	s_cmpk_gt_u32 s11, 0x124f
	s_cbranch_scc0 .LBB0_36
	s_cmpk_gt_u32 s11, 0x144f
	s_cbranch_scc0 .LBB0_33
	s_cmpk_gt_u32 s11, 0x14af
	s_cbranch_scc0 .LBB0_30
	s_cmpk_gt_u32 s11, 0x14ef
	s_cbranch_scc0 .LBB0_27
	v_readlane_b32 s2, v254, 15
	v_lshlrev_b32_e32 v160, 2, v0
	v_add_u32_e32 v86, 0x18c0, v37
	v_mov_b32_e32 v47, s2
	v_readlane_b32 s2, v254, 16
	ds_read_b32 v47, v47
	v_add_u32_e32 v87, 0x18c8, v37
	v_mov_b32_e32 v48, s2
	ds_read_b32 v48, v48
	s_lshl_b64 s[2:3], s[18:19], 2
	s_waitcnt lgkmcnt(1)
	v_readfirstlane_b32 s22, v47
	v_add_u32_e32 v47, 0x14a8, v37
	v_add_u32_e32 v88, 0x1ce0, v37
	s_waitcnt lgkmcnt(0)
	v_readfirstlane_b32 s23, v48
	s_add_u32 s22, s22, s2
	s_addc_u32 s3, s23, s3
	s_add_i32 s2, s11, 0xeb10
	s_lshl_b32 s23, s2, 1
	s_lshl_b32 s2, s2, 5
	s_and_b32 s2, s2, 0x3e0
	s_and_b32 s31, s23, 0x7fc0
	s_lshl_b32 s23, s2, 2
	v_add_u32_e32 v48, s31, v1
	s_add_u32 s22, s22, s23
	s_addc_u32 s23, s3, 0
	v_ashrrev_i32_e32 v49, 31, v48
	v_lshl_add_u64 v[50:51], s[22:23], 0, v[160:161]
	v_lshlrev_b64 v[48:49], 12, v[48:49]
	v_lshl_add_u64 v[76:77], v[50:51], 0, v[48:49]
	s_mov_b32 s3, 0x8000
	v_add_co_u32_e32 v52, vcc, s3, v76
	s_mov_b32 s3, 0x10000
	s_nop 0
	v_addc_co_u32_e32 v53, vcc, 0, v77, vcc
	v_add_co_u32_e32 v56, vcc, s3, v76
	s_mov_b32 s3, 0x18000
	s_nop 0
	v_addc_co_u32_e32 v57, vcc, 0, v77, vcc
	v_add_co_u32_e32 v60, vcc, s3, v76
	s_mov_b32 s3, 0x20000
	s_nop 0
	v_addc_co_u32_e32 v61, vcc, 0, v77, vcc
	v_add_co_u32_e32 v64, vcc, s3, v76
	s_mov_b32 s3, 0x28000
	s_nop 0
	v_addc_co_u32_e32 v65, vcc, 0, v77, vcc
	v_add_co_u32_e32 v68, vcc, s3, v76
	global_load_dwordx4 v[48:51], v[76:77], off nt
	s_nop 0
	global_load_dwordx4 v[52:55], v[52:53], off nt
	v_addc_co_u32_e32 v69, vcc, 0, v77, vcc
	global_load_dwordx4 v[56:59], v[56:57], off nt
	s_nop 0
	global_load_dwordx4 v[60:63], v[60:61], off nt
	s_nop 0
	global_load_dwordx4 v[64:67], v[64:65], off nt
	s_nop 0
	global_load_dwordx4 v[68:71], v[68:69], off nt
	s_mov_b32 s3, 0x30000
	v_add_co_u32_e32 v72, vcc, s3, v76
	s_mov_b32 s3, 0x38000
	s_nop 0
	v_addc_co_u32_e32 v73, vcc, 0, v77, vcc
	global_load_dwordx4 v[72:75], v[72:73], off nt
	v_add_co_u32_e32 v76, vcc, s3, v76
	v_add_u32_e32 v89, 0x1ce8, v37
	s_nop 0
	v_addc_co_u32_e32 v77, vcc, 0, v77, vcc
	global_load_dwordx4 v[76:79], v[76:77], off nt
	v_add_u32_e32 v80, s2, v1
	v_ashrrev_i32_e32 v81, 31, v80
	s_lshl_b32 s96, s31, 1
	v_lshlrev_b64 v[80:81], 11, v[80:81]
	v_lshl_add_u64 v[84:85], v[2:3], 0, s[96:97]
	v_add_u32_e32 v82, s2, v32
	v_ashrrev_i32_e32 v83, 31, v82
	s_waitcnt vmcnt(7)
	ds_write2_b32 v37, v48, v49 offset1:1
	ds_write2_b32 v37, v50, v51 offset0:2 offset1:3
	s_waitcnt vmcnt(6)
	ds_write2_b32 v38, v52, v53 offset1:1
	ds_write2_b32 v39, v54, v55 offset1:1
	s_waitcnt vmcnt(5)
	ds_write2_b32 v40, v56, v57 offset1:1
	ds_write2_b32 v41, v58, v59 offset1:1
	s_waitcnt vmcnt(4)
	ds_write2_b32 v42, v60, v61 offset1:1
	ds_write2_b32 v43, v62, v63 offset1:1
	s_waitcnt vmcnt(3)
	ds_write2_b32 v44, v64, v65 offset1:1
	ds_write2_b32 v45, v66, v67 offset1:1
	s_waitcnt vmcnt(2)
	ds_write2_b32 v46, v68, v69 offset1:1
	ds_write2_b32 v47, v70, v71 offset1:1
	s_waitcnt vmcnt(1)
	ds_write2_b32 v86, v72, v73 offset1:1
	ds_write2_b32 v87, v74, v75 offset1:1
	s_waitcnt vmcnt(0)
	ds_write2_b32 v88, v76, v77 offset1:1
	ds_write2_b32 v89, v78, v79 offset1:1
	s_waitcnt lgkmcnt(0)
	ds_read2_b32 v[52:53], v36 offset0:33 offset1:41
	ds_read2_b32 v[54:55], v36 offset1:8
	ds_read2_b32 v[56:57], v36 offset0:66 offset1:74
	ds_read2_b32 v[58:59], v36 offset0:99 offset1:107
	ds_read2_b32 v[60:61], v36 offset0:132 offset1:140
	ds_read2_b32 v[62:63], v36 offset0:165 offset1:173
	ds_read2_b32 v[64:65], v36 offset0:198 offset1:206
	ds_read2_b32 v[66:67], v36 offset0:231 offset1:239
	v_lshl_add_u64 v[68:69], v[84:85], 0, v[80:81]
	s_waitcnt lgkmcnt(6)
	v_cvt_pk_bf16_f32 v48, v54, v52
	s_waitcnt lgkmcnt(4)
	v_cvt_pk_bf16_f32 v49, v56, v58
	s_waitcnt lgkmcnt(2)
	v_cvt_pk_bf16_f32 v50, v60, v62
	s_waitcnt lgkmcnt(0)
	v_cvt_pk_bf16_f32 v51, v64, v66
	global_store_dwordx4 v[68:69], v[48:51], off
	v_cvt_pk_bf16_f32 v52, v55, v53
	v_cvt_pk_bf16_f32 v53, v57, v59
	v_cvt_pk_bf16_f32 v54, v61, v63
	v_cvt_pk_bf16_f32 v55, v65, v67
	v_lshlrev_b64 v[48:49], 11, v[82:83]
	ds_read2_b32 v[56:57], v36 offset0:49 offset1:57
	ds_read2_b32 v[58:59], v36 offset0:16 offset1:24
	ds_read2_b32 v[60:61], v36 offset0:82 offset1:90
	ds_read2_b32 v[62:63], v36 offset0:115 offset1:123
	ds_read2_b32 v[64:65], v36 offset0:148 offset1:156
	ds_read2_b32 v[66:67], v36 offset0:181 offset1:189
	ds_read2_b32 v[68:69], v36 offset0:214 offset1:222
	ds_read2_b32 v[70:71], v36 offset0:247 offset1:255
	v_lshl_add_u64 v[48:49], v[84:85], 0, v[48:49]
	global_store_dwordx4 v[48:49], v[52:55], off
	s_waitcnt lgkmcnt(6)
	v_cvt_pk_bf16_f32 v48, v58, v56
	s_waitcnt lgkmcnt(4)
	v_cvt_pk_bf16_f32 v49, v60, v62
	v_add_u32_e32 v52, s2, v33
	v_ashrrev_i32_e32 v53, 31, v52
	v_lshlrev_b64 v[52:53], 11, v[52:53]
	s_waitcnt lgkmcnt(2)
	v_cvt_pk_bf16_f32 v50, v64, v66
	s_waitcnt lgkmcnt(0)
	v_cvt_pk_bf16_f32 v51, v68, v70
	v_lshl_add_u64 v[52:53], v[84:85], 0, v[52:53]
	global_store_dwordx4 v[52:53], v[48:51], off
	v_add_u32_e32 v52, s2, v35
	v_ashrrev_i32_e32 v53, 31, v52
	v_lshlrev_b64 v[52:53], 11, v[52:53]
	v_cvt_pk_bf16_f32 v48, v59, v57
	v_cvt_pk_bf16_f32 v49, v61, v63
	v_cvt_pk_bf16_f32 v50, v65, v67
	v_cvt_pk_bf16_f32 v51, v69, v71
	v_lshl_add_u64 v[52:53], v[84:85], 0, v[52:53]
	global_store_dwordx4 v[52:53], v[48:51], off
	s_waitcnt lgkmcnt(0)
	s_mov_b64 s[2:3], 0
.LBB0_27:
	s_andn2_b64 vcc, exec, s[2:3]
	s_cbranch_vccnz .LBB0_29
	v_readlane_b32 s2, v254, 17
	v_lshlrev_b32_e32 v160, 2, v0
	v_add_u32_e32 v86, 0x18c0, v37
	v_mov_b32_e32 v47, s2
	v_readlane_b32 s2, v254, 18
	ds_read_b32 v47, v47
	v_add_u32_e32 v87, 0x18c8, v37
	v_mov_b32_e32 v48, s2
	ds_read_b32 v48, v48
	v_add_u32_e32 v88, 0x1ce0, v37
	s_waitcnt lgkmcnt(1)
	v_readfirstlane_b32 s2, v47
	v_add_u32_e32 v47, 0x14a8, v37
	v_add_u32_e32 v89, 0x1ce8, v37
	s_waitcnt lgkmcnt(0)
	v_readfirstlane_b32 s3, v48
	s_add_u32 s22, s2, s34
	s_addc_u32 s3, s3, s35
	s_add_i32 s2, s11, 0xeb50
	s_and_b32 s23, s2, 0xffff
	s_add_i32 s31, s11, 0xeb30
	s_cmp_lt_u32 s23, 32
	s_cselect_b32 s2, s2, s31
	s_cmp_gt_u32 s23, 31
	s_cselect_b32 s31, 64, 0
	s_lshl_b32 s2, s2, 5
	s_and_b32 s2, s2, 0xffe0
	s_lshl_b32 s23, s2, 2
	v_add_u32_e32 v48, s31, v1
	s_add_u32 s22, s22, s23
	s_addc_u32 s23, s3, 0
	v_ashrrev_i32_e32 v49, 31, v48
	v_lshl_add_u64 v[50:51], s[22:23], 0, v[160:161]
	v_lshlrev_b64 v[48:49], 12, v[48:49]
	v_lshl_add_u64 v[76:77], v[50:51], 0, v[48:49]
	s_mov_b32 s3, 0x8000
	v_add_co_u32_e32 v52, vcc, s3, v76
	s_mov_b32 s3, 0x10000
	s_nop 0
	v_addc_co_u32_e32 v53, vcc, 0, v77, vcc
	v_add_co_u32_e32 v56, vcc, s3, v76
	s_mov_b32 s3, 0x18000
	s_nop 0
	v_addc_co_u32_e32 v57, vcc, 0, v77, vcc
	v_add_co_u32_e32 v60, vcc, s3, v76
	s_mov_b32 s3, 0x20000
	s_nop 0
	v_addc_co_u32_e32 v61, vcc, 0, v77, vcc
	v_add_co_u32_e32 v64, vcc, s3, v76
	s_mov_b32 s3, 0x28000
	s_nop 0
	v_addc_co_u32_e32 v65, vcc, 0, v77, vcc
	v_add_co_u32_e32 v68, vcc, s3, v76
	global_load_dwordx4 v[48:51], v[76:77], off nt
	s_nop 0
	global_load_dwordx4 v[52:55], v[52:53], off nt
	v_addc_co_u32_e32 v69, vcc, 0, v77, vcc
	global_load_dwordx4 v[56:59], v[56:57], off nt
	s_nop 0
	global_load_dwordx4 v[60:63], v[60:61], off nt
	s_nop 0
	global_load_dwordx4 v[64:67], v[64:65], off nt
	s_nop 0
	global_load_dwordx4 v[68:71], v[68:69], off nt
	s_mov_b32 s3, 0x30000
	v_add_co_u32_e32 v72, vcc, s3, v76
	s_mov_b32 s3, 0x38000
	s_nop 0
	v_addc_co_u32_e32 v73, vcc, 0, v77, vcc
	global_load_dwordx4 v[72:75], v[72:73], off nt
	v_add_co_u32_e32 v76, vcc, s3, v76
	v_add_u32_e32 v80, s2, v1
	s_nop 0
	v_addc_co_u32_e32 v77, vcc, 0, v77, vcc
	global_load_dwordx4 v[76:79], v[76:77], off nt
	v_ashrrev_i32_e32 v81, 31, v80
	s_lshl_b32 s96, s31, 1
	v_lshlrev_b64 v[80:81], 9, v[80:81]
	v_lshl_add_u64 v[84:85], v[4:5], 0, s[96:97]
	v_add_u32_e32 v82, s2, v32
	v_ashrrev_i32_e32 v83, 31, v82
	s_waitcnt vmcnt(7)
	ds_write2_b32 v37, v48, v49 offset1:1
	ds_write2_b32 v37, v50, v51 offset0:2 offset1:3
	s_waitcnt vmcnt(6)
	ds_write2_b32 v38, v52, v53 offset1:1
	ds_write2_b32 v39, v54, v55 offset1:1
	s_waitcnt vmcnt(5)
	ds_write2_b32 v40, v56, v57 offset1:1
	ds_write2_b32 v41, v58, v59 offset1:1
	s_waitcnt vmcnt(4)
	ds_write2_b32 v42, v60, v61 offset1:1
	ds_write2_b32 v43, v62, v63 offset1:1
	s_waitcnt vmcnt(3)
	ds_write2_b32 v44, v64, v65 offset1:1
	ds_write2_b32 v45, v66, v67 offset1:1
	s_waitcnt vmcnt(2)
	ds_write2_b32 v46, v68, v69 offset1:1
	ds_write2_b32 v47, v70, v71 offset1:1
	s_waitcnt vmcnt(1)
	ds_write2_b32 v86, v72, v73 offset1:1
	ds_write2_b32 v87, v74, v75 offset1:1
	s_waitcnt vmcnt(0)
	ds_write2_b32 v88, v76, v77 offset1:1
	ds_write2_b32 v89, v78, v79 offset1:1
	s_waitcnt lgkmcnt(0)
	ds_read2_b32 v[52:53], v36 offset0:33 offset1:41
	ds_read2_b32 v[54:55], v36 offset1:8
	ds_read2_b32 v[56:57], v36 offset0:66 offset1:74
	ds_read2_b32 v[58:59], v36 offset0:99 offset1:107
	ds_read2_b32 v[60:61], v36 offset0:132 offset1:140
	ds_read2_b32 v[62:63], v36 offset0:165 offset1:173
	ds_read2_b32 v[64:65], v36 offset0:198 offset1:206
	ds_read2_b32 v[66:67], v36 offset0:231 offset1:239
	v_lshl_add_u64 v[68:69], v[84:85], 0, v[80:81]
	s_waitcnt lgkmcnt(6)
	v_cvt_pk_bf16_f32 v48, v54, v52
	s_waitcnt lgkmcnt(4)
	v_cvt_pk_bf16_f32 v49, v56, v58
	s_waitcnt lgkmcnt(2)
	v_cvt_pk_bf16_f32 v50, v60, v62
	s_waitcnt lgkmcnt(0)
	v_cvt_pk_bf16_f32 v51, v64, v66
	global_store_dwordx4 v[68:69], v[48:51], off
	v_cvt_pk_bf16_f32 v52, v55, v53
	v_cvt_pk_bf16_f32 v53, v57, v59
	v_cvt_pk_bf16_f32 v54, v61, v63
	v_cvt_pk_bf16_f32 v55, v65, v67
	v_lshlrev_b64 v[48:49], 9, v[82:83]
	ds_read2_b32 v[56:57], v36 offset0:49 offset1:57
	ds_read2_b32 v[58:59], v36 offset0:16 offset1:24
	ds_read2_b32 v[60:61], v36 offset0:82 offset1:90
	ds_read2_b32 v[62:63], v36 offset0:115 offset1:123
	ds_read2_b32 v[64:65], v36 offset0:148 offset1:156
	ds_read2_b32 v[66:67], v36 offset0:181 offset1:189
	ds_read2_b32 v[68:69], v36 offset0:214 offset1:222
	ds_read2_b32 v[70:71], v36 offset0:247 offset1:255
	v_lshl_add_u64 v[48:49], v[84:85], 0, v[48:49]
	global_store_dwordx4 v[48:49], v[52:55], off
	s_waitcnt lgkmcnt(6)
	v_cvt_pk_bf16_f32 v48, v58, v56
	s_waitcnt lgkmcnt(4)
	v_cvt_pk_bf16_f32 v49, v60, v62
	v_add_u32_e32 v52, s2, v33
	v_ashrrev_i32_e32 v53, 31, v52
	v_lshlrev_b64 v[52:53], 9, v[52:53]
	s_waitcnt lgkmcnt(2)
	v_cvt_pk_bf16_f32 v50, v64, v66
	s_waitcnt lgkmcnt(0)
	v_cvt_pk_bf16_f32 v51, v68, v70
	v_lshl_add_u64 v[52:53], v[84:85], 0, v[52:53]
	global_store_dwordx4 v[52:53], v[48:51], off
	v_add_u32_e32 v52, s2, v35
	v_ashrrev_i32_e32 v53, 31, v52
	v_lshlrev_b64 v[52:53], 9, v[52:53]
	v_cvt_pk_bf16_f32 v48, v59, v57
	v_cvt_pk_bf16_f32 v49, v61, v63
	v_cvt_pk_bf16_f32 v50, v65, v67
	v_cvt_pk_bf16_f32 v51, v69, v71
	v_lshl_add_u64 v[52:53], v[84:85], 0, v[52:53]
	global_store_dwordx4 v[52:53], v[48:51], off
	s_waitcnt lgkmcnt(0)

.LBB0_30:
	s_andn2_b64 vcc, exec, s[2:3]
	s_cbranch_vccnz .LBB0_32
	v_readlane_b32 s2, v254, 19
	v_lshlrev_b32_e32 v160, 2, v0
	v_add_u32_e32 v86, 0x18c0, v37
	v_mov_b32_e32 v47, s2
	v_readlane_b32 s2, v254, 20
	ds_read_b32 v47, v47
	v_add_u32_e32 v87, 0x18c8, v37
	v_mov_b32_e32 v48, s2
	ds_read_b32 v48, v48
	v_add_u32_e32 v88, 0x1ce0, v37
	s_waitcnt lgkmcnt(1)
	v_readfirstlane_b32 s2, v47
	v_add_u32_e32 v89, 0x1ce8, v37
	s_waitcnt lgkmcnt(0)
	v_readfirstlane_b32 s3, v48
	s_add_u32 s2, s2, s40
	s_addc_u32 s3, s3, s41
	s_add_i32 s22, s11, 0xffb0
	s_and_b32 s23, s22, 0xff
	s_mulk_i32 s23, 0xab
	s_bfe_u32 s23, s23, 0x4000c
	s_mul_i32 s31, s23, 24
	s_sub_i32 s22, s22, s31
	s_lshl_b32 s22, s22, 5
	s_lshl_b32 s23, s23, 6
	s_and_b32 s22, s22, 0x1fe0
	s_and_b32 s23, s23, 0x3c0
	s_lshl_b32 s31, s22, 2
	s_add_u32 s2, s2, s31
	v_add_u32_e32 v47, s23, v1
	s_addc_u32 s3, s3, 0
	v_lshl_add_u64 v[76:77], s[2:3], 0, v[160:161]
	s_movk_i32 s31, 0xc00
	v_add_u32_e32 v50, 8, v47
	v_add_u32_e32 v56, 16, v47
	v_add_u32_e32 v58, 24, v47
	v_add_u32_e32 v64, 32, v47
	v_add_u32_e32 v66, 40, v47
	v_mad_i64_i32 v[48:49], s[2:3], v47, s31, v[76:77]
	v_mad_i64_i32 v[52:53], s[2:3], v50, s31, v[76:77]
	v_mad_i64_i32 v[56:57], s[2:3], v56, s31, v[76:77]
	v_mad_i64_i32 v[60:61], s[2:3], v58, s31, v[76:77]
	v_mad_i64_i32 v[64:65], s[2:3], v64, s31, v[76:77]
	v_mad_i64_i32 v[68:69], s[2:3], v66, s31, v[76:77]
	global_load_dwordx4 v[48:51], v[48:49], off nt
	s_nop 0
	global_load_dwordx4 v[52:55], v[52:53], off nt
	s_nop 0
	global_load_dwordx4 v[56:59], v[56:57], off nt
	s_nop 0
	global_load_dwordx4 v[60:63], v[60:61], off nt
	s_nop 0
	global_load_dwordx4 v[64:67], v[64:65], off nt
	s_nop 0
	global_load_dwordx4 v[68:71], v[68:69], off nt
	v_add_u32_e32 v72, 48, v47
	v_mad_i64_i32 v[72:73], s[2:3], v72, s31, v[76:77]
	global_load_dwordx4 v[72:75], v[72:73], off nt
	v_add_u32_e32 v47, 56, v47
	v_mad_i64_i32 v[76:77], s[2:3], v47, s31, v[76:77]
	global_load_dwordx4 v[76:79], v[76:77], off nt
	v_add_u32_e32 v47, 0x14a8, v37
	v_add_u32_e32 v80, s22, v1
	v_ashrrev_i32_e32 v81, 31, v80
	s_lshl_b32 s96, s23, 1
	v_lshlrev_b64 v[80:81], 9, v[80:81]
	v_lshl_add_u64 v[84:85], v[6:7], 0, s[96:97]
	v_add_u32_e32 v82, s22, v32
	v_lshl_add_u64 v[80:81], v[84:85], 0, v[80:81]
	v_ashrrev_i32_e32 v83, 31, v82
	v_lshlrev_b64 v[82:83], 9, v[82:83]
	v_lshl_add_u64 v[82:83], v[84:85], 0, v[82:83]
	s_waitcnt vmcnt(7)
	ds_write2_b32 v37, v48, v49 offset1:1
	ds_write2_b32 v37, v50, v51 offset0:2 offset1:3
	s_waitcnt vmcnt(6)
	ds_write2_b32 v38, v52, v53 offset1:1
	ds_write2_b32 v39, v54, v55 offset1:1
	s_waitcnt vmcnt(5)
	ds_write2_b32 v40, v56, v57 offset1:1
	ds_write2_b32 v41, v58, v59 offset1:1
	s_waitcnt vmcnt(4)
	ds_write2_b32 v42, v60, v61 offset1:1
	ds_write2_b32 v43, v62, v63 offset1:1
	s_waitcnt vmcnt(3)
	ds_write2_b32 v44, v64, v65 offset1:1
	ds_write2_b32 v45, v66, v67 offset1:1
	s_waitcnt vmcnt(2)
	ds_write2_b32 v46, v68, v69 offset1:1
	ds_write2_b32 v47, v70, v71 offset1:1
	s_waitcnt vmcnt(1)
	ds_write2_b32 v86, v72, v73 offset1:1
	ds_write2_b32 v87, v74, v75 offset1:1
	s_waitcnt vmcnt(0)
	ds_write2_b32 v88, v76, v77 offset1:1
	ds_write2_b32 v89, v78, v79 offset1:1
	s_waitcnt lgkmcnt(0)
	ds_read2_b32 v[52:53], v36 offset0:33 offset1:41
	ds_read2_b32 v[54:55], v36 offset1:8
	ds_read2_b32 v[56:57], v36 offset0:66 offset1:74
	ds_read2_b32 v[58:59], v36 offset0:99 offset1:107
	ds_read2_b32 v[60:61], v36 offset0:132 offset1:140
	ds_read2_b32 v[62:63], v36 offset0:165 offset1:173
	ds_read2_b32 v[64:65], v36 offset0:198 offset1:206
	ds_read2_b32 v[66:67], v36 offset0:231 offset1:239
	ds_read2_b32 v[68:69], v36 offset0:49 offset1:57
	ds_read2_b32 v[70:71], v36 offset0:16 offset1:24
	ds_read2_b32 v[72:73], v36 offset0:82 offset1:90
	ds_read2_b32 v[74:75], v36 offset0:115 offset1:123
	ds_read2_b32 v[76:77], v36 offset0:148 offset1:156
	ds_read2_b32 v[78:79], v36 offset0:181 offset1:189
	s_waitcnt lgkmcnt(12)
	v_cvt_pk_bf16_f32 v48, v54, v52
	s_waitcnt lgkmcnt(10)
	v_cvt_pk_bf16_f32 v49, v56, v58
	s_waitcnt lgkmcnt(8)
	v_cvt_pk_bf16_f32 v50, v60, v62
	s_waitcnt lgkmcnt(6)
	v_cvt_pk_bf16_f32 v51, v64, v66
	global_store_dwordx4 v[80:81], v[48:51], off
	v_cvt_pk_bf16_f32 v52, v55, v53
	v_cvt_pk_bf16_f32 v53, v57, v59
	ds_read2_b32 v[56:57], v36 offset0:214 offset1:222
	ds_read2_b32 v[58:59], v36 offset0:247 offset1:255
	v_cvt_pk_bf16_f32 v54, v61, v63
	v_cvt_pk_bf16_f32 v55, v65, v67
	global_store_dwordx4 v[82:83], v[52:55], off
	s_waitcnt lgkmcnt(6)
	v_cvt_pk_bf16_f32 v48, v70, v68
	s_waitcnt lgkmcnt(4)
	v_cvt_pk_bf16_f32 v49, v72, v74
	v_add_u32_e32 v52, s22, v33
	v_ashrrev_i32_e32 v53, 31, v52
	v_lshlrev_b64 v[52:53], 9, v[52:53]
	s_waitcnt lgkmcnt(2)
	v_cvt_pk_bf16_f32 v50, v76, v78
	s_waitcnt lgkmcnt(0)
	v_cvt_pk_bf16_f32 v51, v56, v58
	v_lshl_add_u64 v[52:53], v[84:85], 0, v[52:53]
	global_store_dwordx4 v[52:53], v[48:51], off
	v_add_u32_e32 v52, s22, v35
	v_ashrrev_i32_e32 v53, 31, v52
	v_lshlrev_b64 v[52:53], 9, v[52:53]
	v_cvt_pk_bf16_f32 v48, v71, v69
	v_cvt_pk_bf16_f32 v49, v73, v75
	v_cvt_pk_bf16_f32 v50, v77, v79
	v_cvt_pk_bf16_f32 v51, v57, v59
	v_lshl_add_u64 v[52:53], v[84:85], 0, v[52:53]
	global_store_dwordx4 v[52:53], v[48:51], off
	s_waitcnt lgkmcnt(0)

.LBB0_33:
	s_andn2_b64 vcc, exec, s[2:3]
	s_cbranch_vccnz .LBB0_35
	v_readlane_b32 s2, v254, 21
	v_lshlrev_b32_e32 v160, 2, v0
	v_add_u32_e32 v86, 0x18c0, v37
	v_mov_b32_e32 v47, s2
	v_readlane_b32 s2, v254, 22
	ds_read_b32 v47, v47
	v_add_u32_e32 v87, 0x18c8, v37
	v_mov_b32_e32 v48, s2
	ds_read_b32 v48, v48
	s_lshl_b64 s[2:3], s[18:19], 2
	s_waitcnt lgkmcnt(1)
	v_readfirstlane_b32 s22, v47
	v_add_u32_e32 v47, 0x14a8, v37
	v_add_u32_e32 v88, 0x1ce0, v37
	s_waitcnt lgkmcnt(0)
	v_readfirstlane_b32 s23, v48
	s_add_u32 s22, s22, s2
	s_addc_u32 s3, s23, s3
	s_add_i32 s2, s11, 0xedb0
	s_lshl_b32 s23, s2, 1
	s_lshl_b32 s2, s2, 5
	s_and_b32 s2, s2, 0x3e0
	s_and_b32 s31, s23, 0x7fc0
	s_lshl_b32 s23, s2, 2
	v_add_u32_e32 v48, s31, v1
	s_add_u32 s22, s22, s23
	s_addc_u32 s23, s3, 0
	v_ashrrev_i32_e32 v49, 31, v48
	v_lshl_add_u64 v[50:51], s[22:23], 0, v[160:161]
	v_lshlrev_b64 v[48:49], 12, v[48:49]
	v_lshl_add_u64 v[76:77], v[50:51], 0, v[48:49]
	s_mov_b32 s3, 0x8000
	v_add_co_u32_e32 v52, vcc, s3, v76
	s_mov_b32 s3, 0x10000
	s_nop 0
	v_addc_co_u32_e32 v53, vcc, 0, v77, vcc
	v_add_co_u32_e32 v56, vcc, s3, v76
	s_mov_b32 s3, 0x18000
	s_nop 0
	v_addc_co_u32_e32 v57, vcc, 0, v77, vcc
	v_add_co_u32_e32 v60, vcc, s3, v76
	s_mov_b32 s3, 0x20000
	s_nop 0
	v_addc_co_u32_e32 v61, vcc, 0, v77, vcc
	v_add_co_u32_e32 v64, vcc, s3, v76
	s_mov_b32 s3, 0x28000
	s_nop 0
	v_addc_co_u32_e32 v65, vcc, 0, v77, vcc
	v_add_co_u32_e32 v68, vcc, s3, v76
	global_load_dwordx4 v[48:51], v[76:77], off nt
	s_nop 0
	global_load_dwordx4 v[52:55], v[52:53], off nt
	v_addc_co_u32_e32 v69, vcc, 0, v77, vcc
	global_load_dwordx4 v[56:59], v[56:57], off nt
	s_nop 0
	global_load_dwordx4 v[60:63], v[60:61], off nt
	s_nop 0
	global_load_dwordx4 v[64:67], v[64:65], off nt
	s_nop 0
	global_load_dwordx4 v[68:71], v[68:69], off nt
	s_mov_b32 s3, 0x30000
	v_add_co_u32_e32 v72, vcc, s3, v76
	s_mov_b32 s3, 0x38000
	s_nop 0
	v_addc_co_u32_e32 v73, vcc, 0, v77, vcc
	global_load_dwordx4 v[72:75], v[72:73], off nt
	v_add_co_u32_e32 v76, vcc, s3, v76
	v_add_u32_e32 v89, 0x1ce8, v37
	s_nop 0
	v_addc_co_u32_e32 v77, vcc, 0, v77, vcc
	global_load_dwordx4 v[76:79], v[76:77], off nt
	v_add_u32_e32 v80, s2, v1
	v_ashrrev_i32_e32 v81, 31, v80
	s_lshl_b32 s96, s31, 1
	v_lshlrev_b64 v[80:81], 11, v[80:81]
	v_lshl_add_u64 v[84:85], v[8:9], 0, s[96:97]
	v_add_u32_e32 v82, s2, v32
	v_ashrrev_i32_e32 v83, 31, v82
	s_waitcnt vmcnt(7)
	ds_write2_b32 v37, v48, v49 offset1:1
	ds_write2_b32 v37, v50, v51 offset0:2 offset1:3
	s_waitcnt vmcnt(6)
	ds_write2_b32 v38, v52, v53 offset1:1
	ds_write2_b32 v39, v54, v55 offset1:1
	s_waitcnt vmcnt(5)
	ds_write2_b32 v40, v56, v57 offset1:1
	ds_write2_b32 v41, v58, v59 offset1:1
	s_waitcnt vmcnt(4)
	ds_write2_b32 v42, v60, v61 offset1:1
	ds_write2_b32 v43, v62, v63 offset1:1
	s_waitcnt vmcnt(3)
	ds_write2_b32 v44, v64, v65 offset1:1
	ds_write2_b32 v45, v66, v67 offset1:1
	s_waitcnt vmcnt(2)
	ds_write2_b32 v46, v68, v69 offset1:1
	ds_write2_b32 v47, v70, v71 offset1:1
	s_waitcnt vmcnt(1)
	ds_write2_b32 v86, v72, v73 offset1:1
	ds_write2_b32 v87, v74, v75 offset1:1
	s_waitcnt vmcnt(0)
	ds_write2_b32 v88, v76, v77 offset1:1
	ds_write2_b32 v89, v78, v79 offset1:1
	s_waitcnt lgkmcnt(0)
	ds_read2_b32 v[52:53], v36 offset0:33 offset1:41
	ds_read2_b32 v[54:55], v36 offset1:8
	ds_read2_b32 v[56:57], v36 offset0:66 offset1:74
	ds_read2_b32 v[58:59], v36 offset0:99 offset1:107
	ds_read2_b32 v[60:61], v36 offset0:132 offset1:140
	ds_read2_b32 v[62:63], v36 offset0:165 offset1:173
	ds_read2_b32 v[64:65], v36 offset0:198 offset1:206
	ds_read2_b32 v[66:67], v36 offset0:231 offset1:239
	v_lshl_add_u64 v[68:69], v[84:85], 0, v[80:81]
	s_waitcnt lgkmcnt(6)
	v_cvt_pk_bf16_f32 v48, v54, v52
	s_waitcnt lgkmcnt(4)
	v_cvt_pk_bf16_f32 v49, v56, v58
	s_waitcnt lgkmcnt(2)
	v_cvt_pk_bf16_f32 v50, v60, v62
	s_waitcnt lgkmcnt(0)
	v_cvt_pk_bf16_f32 v51, v64, v66
	global_store_dwordx4 v[68:69], v[48:51], off
	v_cvt_pk_bf16_f32 v52, v55, v53
	v_cvt_pk_bf16_f32 v53, v57, v59
	v_cvt_pk_bf16_f32 v54, v61, v63
	v_cvt_pk_bf16_f32 v55, v65, v67
	v_lshlrev_b64 v[48:49], 11, v[82:83]
	ds_read2_b32 v[56:57], v36 offset0:49 offset1:57
	ds_read2_b32 v[58:59], v36 offset0:16 offset1:24
	ds_read2_b32 v[60:61], v36 offset0:82 offset1:90
	ds_read2_b32 v[62:63], v36 offset0:115 offset1:123
	ds_read2_b32 v[64:65], v36 offset0:148 offset1:156
	ds_read2_b32 v[66:67], v36 offset0:181 offset1:189
	ds_read2_b32 v[68:69], v36 offset0:214 offset1:222
	ds_read2_b32 v[70:71], v36 offset0:247 offset1:255
	v_lshl_add_u64 v[48:49], v[84:85], 0, v[48:49]
	global_store_dwordx4 v[48:49], v[52:55], off
	s_waitcnt lgkmcnt(6)
	v_cvt_pk_bf16_f32 v48, v58, v56
	s_waitcnt lgkmcnt(4)
	v_cvt_pk_bf16_f32 v49, v60, v62
	v_add_u32_e32 v52, s2, v33
	v_ashrrev_i32_e32 v53, 31, v52
	v_lshlrev_b64 v[52:53], 11, v[52:53]
	s_waitcnt lgkmcnt(2)
	v_cvt_pk_bf16_f32 v50, v64, v66
	s_waitcnt lgkmcnt(0)
	v_cvt_pk_bf16_f32 v51, v68, v70
	v_lshl_add_u64 v[52:53], v[84:85], 0, v[52:53]
	global_store_dwordx4 v[52:53], v[48:51], off
	v_add_u32_e32 v52, s2, v35
	v_ashrrev_i32_e32 v53, 31, v52
	v_lshlrev_b64 v[52:53], 11, v[52:53]
	v_cvt_pk_bf16_f32 v48, v59, v57
	v_cvt_pk_bf16_f32 v49, v61, v63
	v_cvt_pk_bf16_f32 v50, v65, v67
	v_cvt_pk_bf16_f32 v51, v69, v71
	v_lshl_add_u64 v[52:53], v[84:85], 0, v[52:53]
	global_store_dwordx4 v[52:53], v[48:51], off
	s_waitcnt lgkmcnt(0)

.LBB0_36:
	s_andn2_b64 vcc, exec, s[2:3]
	s_cbranch_vccnz .LBB0_38
	v_readlane_b32 s2, v254, 23
	s_add_i32 s31, s11, 0xfffff1b0
	s_lshr_b32 s33, s31, 8
	v_mov_b32_e32 v47, s2
	v_readlane_b32 s2, v254, 24
	ds_read_b32 v47, v47
	s_add_i32 s96, s33, s6
	v_mov_b32_e32 v48, s2
	ds_read_b32 v48, v48
	s_lshl_b64 s[22:23], s[96:97], 21
	s_waitcnt lgkmcnt(1)
	v_readfirstlane_b32 s2, v47
	v_lshlrev_b32_e32 v160, 2, v0
	v_add_u32_e32 v47, 0x14a8, v37
	s_waitcnt lgkmcnt(0)
	v_readfirstlane_b32 s3, v48
	s_add_u32 s2, s2, s22
	s_addc_u32 s3, s3, s23
	s_and_b32 s23, s31, 31
	s_lshl_b32 s22, s33, 10
	s_lshl_b32 s31, s23, 5
	s_or_b32 s22, s22, s31
	s_lshl_b32 s23, s23, 7
	s_add_u32 s2, s2, s23
	s_addc_u32 s3, s3, 0
	v_lshl_add_u64 v[76:77], s[2:3], 0, v[160:161]
	v_lshl_add_u64 v[48:49], v[76:77], 0, v[14:15]
	global_load_dwordx4 v[48:51], v[48:49], off nt
	v_lshl_add_u64 v[52:53], v[76:77], 0, v[16:17]
	global_load_dwordx4 v[52:55], v[52:53], off nt
	v_lshl_add_u64 v[56:57], v[76:77], 0, v[18:19]
	global_load_dwordx4 v[56:59], v[56:57], off nt
	v_lshl_add_u64 v[60:61], v[76:77], 0, v[20:21]
	global_load_dwordx4 v[60:63], v[60:61], off nt
	v_lshl_add_u64 v[64:65], v[76:77], 0, v[22:23]
	global_load_dwordx4 v[64:67], v[64:65], off nt
	v_lshl_add_u64 v[68:69], v[76:77], 0, v[24:25]
	global_load_dwordx4 v[68:71], v[68:69], off nt
	v_lshl_add_u64 v[72:73], v[76:77], 0, v[26:27]
	global_load_dwordx4 v[72:75], v[72:73], off nt
	v_lshl_add_u64 v[76:77], v[76:77], 0, v[28:29]
	global_load_dwordx4 v[76:79], v[76:77], off nt
	v_add_u32_e32 v86, 0x18c0, v37
	v_add_u32_e32 v87, 0x18c8, v37
	v_add_u32_e32 v88, 0x1ce0, v37
	v_add_u32_e32 v89, 0x1ce8, v37
	v_add_u32_e32 v80, s22, v1
	v_add_u32_e32 v82, s22, v32
	v_add_u32_e32 v84, s22, v33
	v_ashrrev_i32_e32 v81, 31, v80
	v_ashrrev_i32_e32 v83, 31, v82
	v_ashrrev_i32_e32 v85, 31, v84
	v_lshlrev_b64 v[80:81], 10, v[80:81]
	v_lshlrev_b64 v[82:83], 10, v[82:83]
	v_lshlrev_b64 v[84:85], 10, v[84:85]
	v_lshl_add_u64 v[80:81], v[30:31], 0, v[80:81]
	v_lshl_add_u64 v[82:83], v[30:31], 0, v[82:83]
	v_lshl_add_u64 v[84:85], v[30:31], 0, v[84:85]
	s_waitcnt vmcnt(7)
	ds_write2_b32 v37, v48, v49 offset1:1
	ds_write2_b32 v37, v50, v51 offset0:2 offset1:3
	s_waitcnt vmcnt(6)
	ds_write2_b32 v38, v52, v53 offset1:1
	ds_write2_b32 v39, v54, v55 offset1:1
	s_waitcnt vmcnt(5)
	ds_write2_b32 v40, v56, v57 offset1:1
	ds_write2_b32 v41, v58, v59 offset1:1
	s_waitcnt vmcnt(4)
	ds_write2_b32 v42, v60, v61 offset1:1
	ds_write2_b32 v43, v62, v63 offset1:1
	s_waitcnt vmcnt(3)
	ds_write2_b32 v44, v64, v65 offset1:1
	ds_write2_b32 v45, v66, v67 offset1:1
	s_waitcnt vmcnt(2)
	ds_write2_b32 v46, v68, v69 offset1:1
	ds_write2_b32 v47, v70, v71 offset1:1
	s_waitcnt vmcnt(1)
	ds_write2_b32 v86, v72, v73 offset1:1
	ds_write2_b32 v87, v74, v75 offset1:1
	s_waitcnt vmcnt(0)
	ds_write2_b32 v88, v76, v77 offset1:1
	ds_write2_b32 v89, v78, v79 offset1:1
	s_waitcnt lgkmcnt(0)
	ds_read2_b32 v[52:53], v36 offset0:33 offset1:41
	ds_read2_b32 v[54:55], v36 offset1:8
	ds_read2_b32 v[56:57], v36 offset0:66 offset1:74
	ds_read2_b32 v[58:59], v36 offset0:99 offset1:107
	ds_read2_b32 v[60:61], v36 offset0:132 offset1:140
	ds_read2_b32 v[62:63], v36 offset0:165 offset1:173
	ds_read2_b32 v[64:65], v36 offset0:198 offset1:206
	ds_read2_b32 v[66:67], v36 offset0:231 offset1:239
	ds_read2_b32 v[68:69], v36 offset0:49 offset1:57
	ds_read2_b32 v[70:71], v36 offset0:16 offset1:24
	ds_read2_b32 v[72:73], v36 offset0:82 offset1:90
	ds_read2_b32 v[74:75], v36 offset0:115 offset1:123
	ds_read2_b32 v[76:77], v36 offset0:148 offset1:156
	ds_read2_b32 v[78:79], v36 offset0:181 offset1:189
	ds_read2_b32 v[86:87], v36 offset0:214 offset1:222
	ds_read2_b32 v[88:89], v36 offset0:247 offset1:255
	s_waitcnt lgkmcnt(14)
	v_cvt_pk_bf16_f32 v48, v54, v52
	s_waitcnt lgkmcnt(12)
	v_cvt_pk_bf16_f32 v49, v56, v58
	s_waitcnt lgkmcnt(10)
	v_cvt_pk_bf16_f32 v50, v60, v62
	s_waitcnt lgkmcnt(8)
	v_cvt_pk_bf16_f32 v51, v64, v66
	v_cvt_pk_bf16_f32 v52, v55, v53
	v_cvt_pk_bf16_f32 v53, v57, v59
	v_cvt_pk_bf16_f32 v54, v61, v63
	v_cvt_pk_bf16_f32 v55, v65, v67
	s_waitcnt lgkmcnt(6)
	v_cvt_pk_bf16_f32 v56, v70, v68
	s_waitcnt lgkmcnt(4)
	v_cvt_pk_bf16_f32 v57, v72, v74
	s_waitcnt lgkmcnt(2)
	v_cvt_pk_bf16_f32 v58, v76, v78
	s_waitcnt lgkmcnt(0)
	v_cvt_pk_bf16_f32 v59, v86, v88
	global_store_dwordx4 v[80:81], v[48:51], off
	global_store_dwordx4 v[82:83], v[52:55], off
	global_store_dwordx4 v[84:85], v[56:59], off
	v_add_u32_e32 v48, s22, v35
	v_ashrrev_i32_e32 v49, 31, v48
	v_lshlrev_b64 v[48:49], 10, v[48:49]
	v_cvt_pk_bf16_f32 v60, v71, v69
	v_cvt_pk_bf16_f32 v61, v73, v75
	v_cvt_pk_bf16_f32 v62, v77, v79
	v_cvt_pk_bf16_f32 v63, v87, v89
	v_lshl_add_u64 v[48:49], v[30:31], 0, v[48:49]
	global_store_dwordx4 v[48:49], v[60:63], off
	s_waitcnt lgkmcnt(0)

.LBB0_39:
	s_andn2_b64 vcc, exec, s[2:3]
	s_cbranch_vccnz .LBB0_41
	v_readlane_b32 s2, v254, 25
	v_lshlrev_b32_e32 v160, 2, v0
	s_mov_b32 s4, 0x42000000
	v_mov_b32_e32 v47, s2
	v_readlane_b32 s2, v254, 26
	ds_read_b32 v47, v47
	v_add_u32_e32 v80, 0x18c0, v37
	v_mov_b32_e32 v48, s2
	ds_read_b32 v48, v48
	s_add_i32 s2, s11, 0xfffff9b0
	s_lshr_b32 s31, s2, 9
	s_add_i32 s96, s31, s6
	s_waitcnt lgkmcnt(1)
	v_readfirstlane_b32 s2, v47
	s_waitcnt lgkmcnt(0)
	v_readfirstlane_b32 s3, v48
	s_lshl_b64 s[22:23], s[96:97], 22
	s_add_u32 s22, s2, s22
	s_addc_u32 s3, s3, s23
	s_add_i32 s2, s7, 0xffff3600
	s_and_b32 s23, s2, 0x3e0
	s_lshl_b32 s2, s31, 10
	s_and_b32 s96, s10, 0x3c0
	s_or_b32 s2, s23, s2
	s_lshl_b32 s23, s23, 2
	v_add_u32_e32 v48, s96, v1
	s_add_u32 s22, s22, s23
	s_addc_u32 s23, s3, 0
	v_ashrrev_i32_e32 v49, 31, v48
	v_lshl_add_u64 v[50:51], s[22:23], 0, v[160:161]
	v_lshlrev_b64 v[48:49], 12, v[48:49]
	v_lshl_add_u64 v[76:77], v[50:51], 0, v[48:49]
	s_mov_b32 s3, 0x8000
	v_add_co_u32_e32 v52, vcc, s3, v76
	s_mov_b32 s3, 0x10000
	s_nop 0
	v_addc_co_u32_e32 v53, vcc, 0, v77, vcc
	v_add_co_u32_e32 v56, vcc, s3, v76
	s_mov_b32 s3, 0x18000
	s_nop 0
	v_addc_co_u32_e32 v57, vcc, 0, v77, vcc
	v_add_co_u32_e32 v60, vcc, s3, v76
	s_mov_b32 s3, 0x20000
	s_nop 0
	v_addc_co_u32_e32 v61, vcc, 0, v77, vcc
	v_add_co_u32_e32 v64, vcc, s3, v76
	s_mov_b32 s3, 0x28000
	s_nop 0
	v_addc_co_u32_e32 v65, vcc, 0, v77, vcc
	v_add_co_u32_e32 v68, vcc, s3, v76
	s_mov_b32 s3, 0x30000
	s_nop 0
	v_addc_co_u32_e32 v69, vcc, 0, v77, vcc
	v_add_co_u32_e32 v72, vcc, s3, v76
	s_mov_b32 s3, 0x38000
	s_nop 0
	v_addc_co_u32_e32 v73, vcc, 0, v77, vcc
	global_load_dwordx4 v[48:51], v[76:77], off nt
	s_nop 0
	global_load_dwordx4 v[52:55], v[52:53], off nt
	v_add_co_u32_e32 v76, vcc, s3, v76
	global_load_dwordx4 v[56:59], v[56:57], off nt
	s_nop 0
	global_load_dwordx4 v[60:63], v[60:61], off nt
	v_addc_co_u32_e32 v77, vcc, 0, v77, vcc
	global_load_dwordx4 v[64:67], v[64:65], off nt
	s_nop 0
	global_load_dwordx4 v[68:71], v[68:69], off nt
	v_add_u32_e32 v47, 0x14a8, v37
	global_load_dwordx4 v[72:75], v[72:73], off nt
	v_add_u32_e32 v81, 0x18c8, v37
	global_load_dwordx4 v[76:79], v[76:77], off nt
	v_add_u32_e32 v82, 0x1ce0, v37
	v_add_u32_e32 v83, 0x1ce8, v37
	s_waitcnt vmcnt(7)
	v_pk_mul_f32 v[48:49], v[48:49], s[4:5] op_sel_hi:[1,0]
	v_pk_mul_f32 v[50:51], v[50:51], s[4:5] op_sel_hi:[1,0]
	ds_write2_b32 v37, v48, v49 offset1:1
	ds_write2_b32 v37, v50, v51 offset0:2 offset1:3
	s_waitcnt vmcnt(6)
	v_pk_mul_f32 v[48:49], v[52:53], s[4:5] op_sel_hi:[1,0]
	v_pk_mul_f32 v[50:51], v[54:55], s[4:5] op_sel_hi:[1,0]
	s_waitcnt vmcnt(5)
	v_pk_mul_f32 v[52:53], v[56:57], s[4:5] op_sel_hi:[1,0]
	v_pk_mul_f32 v[54:55], v[58:59], s[4:5] op_sel_hi:[1,0]
	s_waitcnt vmcnt(4)
	v_pk_mul_f32 v[56:57], v[60:61], s[4:5] op_sel_hi:[1,0]
	v_pk_mul_f32 v[58:59], v[62:63], s[4:5] op_sel_hi:[1,0]
	s_waitcnt vmcnt(3)
	v_pk_mul_f32 v[60:61], v[64:65], s[4:5] op_sel_hi:[1,0]
	v_pk_mul_f32 v[62:63], v[66:67], s[4:5] op_sel_hi:[1,0]
	s_waitcnt vmcnt(2)
	v_pk_mul_f32 v[64:65], v[68:69], s[4:5] op_sel_hi:[1,0]
	v_pk_mul_f32 v[66:67], v[70:71], s[4:5] op_sel_hi:[1,0]
	s_waitcnt vmcnt(1)
	v_pk_mul_f32 v[68:69], v[72:73], s[4:5] op_sel_hi:[1,0]
	v_pk_mul_f32 v[70:71], v[74:75], s[4:5] op_sel_hi:[1,0]
	s_waitcnt vmcnt(0)
	v_pk_mul_f32 v[72:73], v[76:77], s[4:5] op_sel_hi:[1,0]
	v_pk_mul_f32 v[74:75], v[78:79], s[4:5] op_sel_hi:[1,0]
	ds_write2_b32 v38, v48, v49 offset1:1
	ds_write2_b32 v39, v50, v51 offset1:1
	ds_write2_b32 v40, v52, v53 offset1:1
	ds_write2_b32 v41, v54, v55 offset1:1
	ds_write2_b32 v42, v56, v57 offset1:1
	ds_write2_b32 v43, v58, v59 offset1:1
	ds_write2_b32 v44, v60, v61 offset1:1
	ds_write2_b32 v45, v62, v63 offset1:1
	ds_write2_b32 v46, v64, v65 offset1:1
	ds_write2_b32 v47, v66, v67 offset1:1
	ds_write2_b32 v80, v68, v69 offset1:1
	ds_write2_b32 v81, v70, v71 offset1:1
	ds_write2_b32 v82, v72, v73 offset1:1
	ds_write2_b32 v83, v74, v75 offset1:1
	s_waitcnt lgkmcnt(0)
	ds_read2_b32 v[48:49], v36 offset0:33 offset1:41
	ds_read2_b32 v[50:51], v36 offset0:66 offset1:74
	ds_read2_b32 v[52:53], v36 offset1:8
	ds_read2_b32 v[54:55], v36 offset0:99 offset1:107
	ds_read2_b32 v[58:59], v36 offset0:132 offset1:140
	ds_read2_b32 v[60:61], v36 offset0:165 offset1:173
	v_mov_b32_e32 v56, v161
	ds_read2_b32 v[62:63], v36 offset0:198 offset1:206
	ds_read2_b32 v[64:65], v36 offset0:231 offset1:239
	v_mov_b32_e32 v57, v161
	s_waitcnt lgkmcnt(5)
	v_cvt_pk_fp8_f32 v56, v52, v48
	s_waitcnt lgkmcnt(2)
	v_cvt_pk_fp8_f32 v57, v58, v60
	v_mov_b32_e32 v48, v161
	v_add_u32_e32 v68, s2, v1
	v_cvt_pk_fp8_f32 v56, v50, v54 op_sel:[0,0,1]
	s_waitcnt lgkmcnt(0)
	v_cvt_pk_fp8_f32 v57, v62, v64 op_sel:[0,0,1]
	v_cvt_pk_fp8_f32 v48, v53, v49
	v_mov_b32_e32 v49, v161
	v_ashrrev_i32_e32 v69, 31, v68
	v_cvt_pk_fp8_f32 v49, v59, v61
	v_lshl_add_u64 v[66:67], v[10:11], 0, s[96:97]
	v_lshlrev_b64 v[68:69], 10, v[68:69]
	v_lshl_add_u64 v[52:53], v[66:67], 0, v[68:69]
	global_store_dwordx2 v[52:53], v[56:57], off
	v_cvt_pk_fp8_f32 v48, v51, v55 op_sel:[0,0,1]
	v_cvt_pk_fp8_f32 v49, v63, v65 op_sel:[0,0,1]
	ds_read2_b32 v[52:53], v36 offset0:49 offset1:57
	ds_read2_b32 v[54:55], v36 offset0:82 offset1:90
	ds_read2_b32 v[56:57], v36 offset0:16 offset1:24
	ds_read2_b32 v[58:59], v36 offset0:115 offset1:123
	ds_read2_b32 v[62:63], v36 offset0:148 offset1:156
	ds_read2_b32 v[64:65], v36 offset0:181 offset1:189
	v_add_u32_e32 v50, s2, v32
	v_mov_b32_e32 v60, v161
	ds_read2_b32 v[68:69], v36 offset0:214 offset1:222
	ds_read2_b32 v[70:71], v36 offset0:247 offset1:255
	v_mov_b32_e32 v61, v161
	v_ashrrev_i32_e32 v51, 31, v50
	s_waitcnt lgkmcnt(5)
	v_cvt_pk_fp8_f32 v60, v56, v52
	s_waitcnt lgkmcnt(2)
	v_cvt_pk_fp8_f32 v61, v62, v64
	v_lshlrev_b64 v[50:51], 10, v[50:51]
	v_lshl_add_u64 v[50:51], v[66:67], 0, v[50:51]
	global_store_dwordx2 v[50:51], v[48:49], off
	v_mov_b32_e32 v50, v161
	v_mov_b32_e32 v51, v161
	v_cvt_pk_fp8_f32 v60, v54, v58 op_sel:[0,0,1]
	s_waitcnt lgkmcnt(0)
	v_cvt_pk_fp8_f32 v61, v68, v70 op_sel:[0,0,1]
	v_add_u32_e32 v48, s2, v33
	v_cvt_pk_fp8_f32 v50, v57, v53
	v_cvt_pk_fp8_f32 v51, v63, v65
	v_ashrrev_i32_e32 v49, 31, v48
	v_lshlrev_b64 v[48:49], 10, v[48:49]
	v_lshl_add_u64 v[48:49], v[66:67], 0, v[48:49]
	global_store_dwordx2 v[48:49], v[60:61], off
	v_cvt_pk_fp8_f32 v50, v55, v59 op_sel:[0,0,1]
	v_cvt_pk_fp8_f32 v51, v69, v71 op_sel:[0,0,1]
	v_add_u32_e32 v48, s2, v35
	v_ashrrev_i32_e32 v49, 31, v48
	v_lshlrev_b64 v[48:49], 10, v[48:49]
	v_lshl_add_u64 v[48:49], v[66:67], 0, v[48:49]
	global_store_dwordx2 v[48:49], v[50:51], off
	s_waitcnt lgkmcnt(0)

.LBB0_42:
	s_andn2_b64 vcc, exec, s[2:3]
	s_cbranch_vccnz .LBB0_19
	v_readlane_b32 s22, v254, 27
	s_mul_hi_i32 s2, s11, 0x288df0cb
	s_lshr_b32 s3, s2, 31
	v_mov_b32_e32 v47, s22
	v_readlane_b32 s22, v254, 28
	ds_read_b32 v47, v47
	s_ashr_i32 s2, s2, 4
	v_mov_b32_e32 v48, s22
	ds_read_b32 v48, v48
	s_add_i32 s31, s2, s3
	s_mul_i32 s2, s31, 0xffffff9b
	s_add_i32 s23, s11, s2
	s_waitcnt lgkmcnt(1)
	v_readfirstlane_b32 s2, v47
	s_waitcnt lgkmcnt(0)
	v_readfirstlane_b32 s3, v48
	s_add_u32 s33, s2, s42
	s_mul_i32 s22, s31, 0xfffff360
	s_addc_u32 s3, s3, s43
	s_lshl_b32 s2, s31, 6
	s_add_i32 s22, s7, s22
	s_cmp_gt_i32 s23, 60
	s_cselect_b32 s38, 0x60, 0
	s_ashr_i32 s23, s22, 31
	s_lshl_b64 s[22:23], s[22:23], 2
	s_add_u32 s22, s33, s22
	v_add_u32_e32 v47, s2, v1
	s_addc_u32 s23, s3, s23
	v_lshlrev_b32_e32 v160, 2, v0
	v_lshl_add_u64 v[76:77], s[22:23], 0, v[160:161]
	s_movk_i32 s3, 0x3280
	v_add_u32_e32 v50, 8, v47
	v_add_u32_e32 v56, 16, v47
	v_add_u32_e32 v58, 24, v47
	v_add_u32_e32 v64, 32, v47
	v_add_u32_e32 v66, 40, v47
	v_mad_i64_i32 v[48:49], s[22:23], v47, s3, v[76:77]
	v_mad_i64_i32 v[52:53], s[22:23], v50, s3, v[76:77]
	v_mad_i64_i32 v[56:57], s[22:23], v56, s3, v[76:77]
	v_mad_i64_i32 v[60:61], s[22:23], v58, s3, v[76:77]
	v_mad_i64_i32 v[64:65], s[22:23], v64, s3, v[76:77]
	v_mad_i64_i32 v[68:69], s[22:23], v66, s3, v[76:77]
	global_load_dwordx4 v[48:51], v[48:49], off nt
	s_nop 0
	global_load_dwordx4 v[52:55], v[52:53], off nt
	s_nop 0
	global_load_dwordx4 v[56:59], v[56:57], off nt
	s_nop 0
	global_load_dwordx4 v[60:63], v[60:61], off nt
	s_nop 0
	global_load_dwordx4 v[64:67], v[64:65], off nt
	s_nop 0
	global_load_dwordx4 v[68:71], v[68:69], off nt
	v_add_u32_e32 v72, 48, v47
	v_mad_i64_i32 v[72:73], s[22:23], v72, s3, v[76:77]
	global_load_dwordx4 v[72:75], v[72:73], off nt
	v_add_u32_e32 v47, 56, v47
	v_mad_i64_i32 v[76:77], s[22:23], v47, s3, v[76:77]
	global_load_dwordx4 v[76:79], v[76:77], off nt
	v_add_u32_e32 v47, 0x14a8, v37
	v_add_u32_e32 v86, 0x18c0, v37
	v_add_u32_e32 v87, 0x18c8, v37
	v_add_u32_e32 v88, 0x1ce0, v37
	v_add_u32_e32 v89, 0x1ce8, v37
	s_mulk_i32 s31, 0xca0
	s_sub_i32 s22, s38, s31
	s_add_i32 s22, s22, s7
	v_add_u32_e32 v82, s22, v1
	s_ashr_i32 s3, s2, 31
	v_ashrrev_i32_e32 v83, 31, v82
	v_lshl_add_u64 v[80:81], s[2:3], 1, v[12:13]
	v_lshlrev_b64 v[84:85], 11, v[82:83]
	s_mov_b32 s38, 0x6dc9c883
	s_mov_b32 s39, 0x3fc45f30
	s_waitcnt vmcnt(7)
	ds_write2_b32 v37, v48, v49 offset1:1
	ds_write2_b32 v37, v50, v51 offset0:2 offset1:3
	s_waitcnt vmcnt(6)
	ds_write2_b32 v38, v52, v53 offset1:1
	ds_write2_b32 v39, v54, v55 offset1:1
	s_waitcnt vmcnt(5)
	ds_write2_b32 v40, v56, v57 offset1:1
	ds_write2_b32 v41, v58, v59 offset1:1
	s_waitcnt vmcnt(4)
	ds_write2_b32 v42, v60, v61 offset1:1
	ds_write2_b32 v43, v62, v63 offset1:1
	s_waitcnt vmcnt(3)
	ds_write2_b32 v44, v64, v65 offset1:1
	ds_write2_b32 v45, v66, v67 offset1:1
	s_waitcnt vmcnt(2)
	ds_write2_b32 v46, v68, v69 offset1:1
	ds_write2_b32 v47, v70, v71 offset1:1
	s_waitcnt vmcnt(1)
	ds_write2_b32 v86, v72, v73 offset1:1
	ds_write2_b32 v87, v74, v75 offset1:1
	s_waitcnt vmcnt(0)
	ds_write2_b32 v88, v76, v77 offset1:1
	ds_write2_b32 v89, v78, v79 offset1:1
	s_waitcnt lgkmcnt(0)
	ds_read2_b32 v[52:53], v36 offset0:33 offset1:41
	ds_read2_b32 v[54:55], v36 offset1:8
	ds_read2_b32 v[56:57], v36 offset0:66 offset1:74
	ds_read2_b32 v[58:59], v36 offset0:99 offset1:107
	ds_read2_b32 v[60:61], v36 offset0:132 offset1:140
	ds_read2_b32 v[62:63], v36 offset0:165 offset1:173
	ds_read2_b32 v[64:65], v36 offset0:198 offset1:206
	ds_read2_b32 v[66:67], v36 offset0:231 offset1:239
	v_lshl_add_u64 v[68:69], v[80:81], 0, v[84:85]
	s_waitcnt lgkmcnt(6)
	v_cvt_pk_bf16_f32 v48, v54, v52
	s_waitcnt lgkmcnt(4)
	v_cvt_pk_bf16_f32 v49, v56, v58
	s_waitcnt lgkmcnt(2)
	v_cvt_pk_bf16_f32 v50, v60, v62
	s_waitcnt lgkmcnt(0)
	v_cvt_pk_bf16_f32 v51, v64, v66
	global_store_dwordx4 v[68:69], v[48:51], off
	v_cvt_pk_bf16_f32 v52, v55, v53
	v_cvt_pk_bf16_f32 v53, v57, v59
	v_add_u32_e32 v48, 8, v82
	v_ashrrev_i32_e32 v49, 31, v48
	v_cvt_pk_bf16_f32 v54, v61, v63
	v_cvt_pk_bf16_f32 v55, v65, v67
	v_lshlrev_b64 v[48:49], 11, v[48:49]
	ds_read2_b32 v[56:57], v36 offset0:49 offset1:57
	ds_read2_b32 v[58:59], v36 offset0:16 offset1:24
	ds_read2_b32 v[60:61], v36 offset0:82 offset1:90
	ds_read2_b32 v[62:63], v36 offset0:115 offset1:123
	ds_read2_b32 v[64:65], v36 offset0:148 offset1:156
	ds_read2_b32 v[66:67], v36 offset0:181 offset1:189
	ds_read2_b32 v[68:69], v36 offset0:214 offset1:222
	ds_read2_b32 v[70:71], v36 offset0:247 offset1:255
	v_lshl_add_u64 v[48:49], v[80:81], 0, v[48:49]
	global_store_dwordx4 v[48:49], v[52:55], off
	s_waitcnt lgkmcnt(6)
	v_cvt_pk_bf16_f32 v48, v58, v56
	s_waitcnt lgkmcnt(4)
	v_cvt_pk_bf16_f32 v49, v60, v62
	v_add_u32_e32 v52, 16, v82
	v_ashrrev_i32_e32 v53, 31, v52
	v_lshlrev_b64 v[52:53], 11, v[52:53]
	s_waitcnt lgkmcnt(2)
	v_cvt_pk_bf16_f32 v50, v64, v66
	s_waitcnt lgkmcnt(0)
	v_cvt_pk_bf16_f32 v51, v68, v70
	v_lshl_add_u64 v[52:53], v[80:81], 0, v[52:53]
	global_store_dwordx4 v[52:53], v[48:51], off
	v_add_u32_e32 v52, 24, v82
	v_ashrrev_i32_e32 v53, 31, v52
	v_lshlrev_b64 v[52:53], 11, v[52:53]
	v_cvt_pk_bf16_f32 v48, v59, v57
	v_cvt_pk_bf16_f32 v49, v61, v63
	v_cvt_pk_bf16_f32 v50, v65, v67
	v_cvt_pk_bf16_f32 v51, v69, v71
	v_lshl_add_u64 v[52:53], v[80:81], 0, v[52:53]
	global_store_dwordx4 v[52:53], v[48:51], off
	s_waitcnt lgkmcnt(0)
	s_branch .LBB0_19

.LBB0_60:
	v_mul_f32_e32 v58, v57, v57
	v_mul_f32_e32 v59, v55, v55
	v_fmac_f32_e32 v58, v56, v56
	v_fmac_f32_e32 v59, v54, v54
	v_add_f32_e32 v58, v58, v59
	v_mul_f32_e32 v59, v53, v53
	v_mul_f32_e32 v60, v51, v51
	v_fmac_f32_e32 v59, v52, v52
	v_fmac_f32_e32 v60, v50, v50
	v_add_f32_e32 v59, v59, v60
	v_add_f32_e32 v58, v58, v59
	v_mul_f32_e32 v59, v49, v49
	v_mul_f32_e32 v60, v47, v47
	v_fmac_f32_e32 v59, v48, v48
	v_fmac_f32_e32 v60, v46, v46
	v_add_f32_e32 v59, v59, v60
	v_add_f32_e32 v58, v59, v58
	v_mul_f32_e32 v59, v45, v45
	v_mul_f32_e32 v60, v43, v43
	v_fmac_f32_e32 v59, v44, v44
	v_fmac_f32_e32 v60, v42, v42
	v_add_f32_e32 v59, v59, v60
	v_add_f32_e32 v58, v59, v58
	v_lshl_add_u64 v[60:61], s[36:37], 0, v[38:39]
	v_add_co_u32_e32 v60, vcc, s7, v60
	v_add_f32_dpp v58, v58, v58 quad_perm:[1,0,3,2] row_mask:0xf bank_mask:0xf bound_ctrl:1
	s_nop 0
	v_addc_co_u32_e32 v61, vcc, 0, v61, vcc
	v_add_f32_dpp v58, v58, v58 quad_perm:[2,3,0,1] row_mask:0xf bank_mask:0xf bound_ctrl:1
	s_mov_b64 s[18:19], 0x800000
	s_addk_i32 s6, 0x800
	v_add_f32_dpp v58, v58, v58 row_half_mirror row_mask:0xf bank_mask:0xf bound_ctrl:1
	v_lshl_add_u64 v[38:39], v[38:39], 0, s[22:23]
	v_lshl_add_u64 v[40:41], v[40:41], 0, s[18:19]
	v_add_f32_dpp v58, v58, v58 row_mirror row_mask:0xf bank_mask:0xf bound_ctrl:1
	v_mov_b32_e32 v59, v58
	s_nop 1
	v_permlane16_swap_b32_e32 v58, v59
	v_add_f32_e32 v58, v58, v59
	v_mov_b32_e32 v59, v58
	s_nop 1
	v_permlane32_swap_b32_e32 v58, v59
	v_add_f32_e32 v58, v58, v59
	v_fmamk_f32 v58, v58, 0x3a800000, v240
	v_rsq_f32_e32 v58, v58
	s_nop 0
	v_pk_mul_f32 v[62:63], v[56:57], v[58:59] op_sel_hi:[1,0]
	v_pk_mul_f32 v[64:65], v[54:55], v[58:59] op_sel_hi:[1,0]
	s_waitcnt vmcnt(3)
	v_pk_mul_f32 v[62:63], v[8:9], v[62:63]
	v_pk_mul_f32 v[64:65], v[10:11], v[64:65]
	v_cvt_pk_bf16_f32 v62, v62, v63
	v_cvt_pk_bf16_f32 v63, v64, v65
	global_store_dwordx2 v[60:61], v[62:63], off
	v_pk_mul_f32 v[62:63], v[52:53], v[58:59] op_sel_hi:[1,0]
	v_pk_mul_f32 v[64:65], v[50:51], v[58:59] op_sel_hi:[1,0]
	s_waitcnt vmcnt(3)
	v_pk_mul_f32 v[62:63], v[16:17], v[62:63]
	v_pk_mul_f32 v[64:65], v[18:19], v[64:65]
	v_cvt_pk_bf16_f32 v62, v62, v63
	v_cvt_pk_bf16_f32 v63, v64, v65
	global_store_dwordx2 v[60:61], v[62:63], off offset:512
	v_pk_mul_f32 v[62:63], v[48:49], v[58:59] op_sel_hi:[1,0]
	v_pk_mul_f32 v[64:65], v[46:47], v[58:59] op_sel_hi:[1,0]
	s_waitcnt vmcnt(3)
	v_pk_mul_f32 v[62:63], v[20:21], v[62:63]
	v_pk_mul_f32 v[64:65], v[22:23], v[64:65]
	v_cvt_pk_bf16_f32 v62, v62, v63
	v_cvt_pk_bf16_f32 v63, v64, v65
	global_store_dwordx2 v[60:61], v[62:63], off offset:1024
	v_pk_mul_f32 v[62:63], v[44:45], v[58:59] op_sel_hi:[1,0]
	v_pk_mul_f32 v[64:65], v[42:43], v[58:59] op_sel_hi:[1,0]
	v_mul_f32_e32 v58, 0x41800000, v58
	v_mul_f32_e32 v56, v56, v58
	v_mul_f32_e32 v57, v57, v58
	v_mul_f32_e32 v56, v8, v56
	v_mul_f32_e32 v57, v9, v57
	v_mov_b32_e32 v59, v161
	v_mul_f32_e32 v52, v52, v58
	v_mul_f32_e32 v53, v53, v58
	v_cvt_pk_fp8_f32 v59, v56, v57
	v_mul_f32_e32 v52, v16, v52
	v_mul_f32_e32 v53, v17, v53
	v_mov_b32_e32 v56, v161
	v_cvt_pk_fp8_f32 v56, v52, v53
	v_mul_f32_e32 v50, v50, v58
	v_mul_f32_e32 v51, v51, v58
	v_mul_f32_e32 v50, v18, v50
	v_mul_f32_e32 v51, v19, v51
	v_mul_f32_e32 v48, v48, v58
	v_mul_f32_e32 v49, v49, v58
	v_cvt_pk_fp8_f32 v56, v50, v51 op_sel:[0,0,1]
	v_mul_f32_e32 v48, v20, v48
	v_mul_f32_e32 v49, v21, v49
	v_mov_b32_e32 v50, v161
	v_cvt_pk_fp8_f32 v50, v48, v49
	v_mul_f32_e32 v46, v46, v58
	v_mul_f32_e32 v47, v47, v58
	v_mul_f32_e32 v46, v22, v46
	v_mul_f32_e32 v47, v23, v47
	v_mul_f32_e32 v44, v44, v58
	v_mul_f32_e32 v45, v45, v58
	v_mul_f32_e32 v54, v54, v58
	v_mul_f32_e32 v55, v55, v58
	v_cvt_pk_fp8_f32 v50, v46, v47 op_sel:[0,0,1]
	s_waitcnt vmcnt(3)
	v_mul_f32_e32 v44, v24, v44
	v_mul_f32_e32 v45, v25, v45
	v_mov_b32_e32 v46, v161
	v_pk_mul_f32 v[62:63], v[24:25], v[62:63]
	v_pk_mul_f32 v[64:65], v[26:27], v[64:65]
	v_mul_f32_e32 v54, v10, v54
	v_mul_f32_e32 v55, v11, v55
	v_cvt_pk_fp8_f32 v46, v44, v45
	v_cvt_pk_bf16_f32 v62, v62, v63
	v_cvt_pk_bf16_f32 v63, v64, v65
	v_cvt_pk_fp8_f32 v59, v54, v55 op_sel:[0,0,1]
	global_store_dwordx2 v[60:61], v[62:63], off offset:1536
	v_lshl_add_u64 v[60:61], s[36:37], 0, v[36:37]
	v_mul_f32_e32 v42, v42, v58
	v_mul_f32_e32 v43, v43, v58
	v_add_co_u32_e32 v54, vcc, s10, v60
	v_mul_f32_e32 v42, v26, v42
	v_mul_f32_e32 v43, v27, v43
	v_addc_co_u32_e32 v55, vcc, 0, v61, vcc
	v_cvt_pk_fp8_f32 v46, v42, v43 op_sel:[0,0,1]
	global_store_dword v[54:55], v59, off
	global_store_dword v[54:55], v56, off offset:256
	global_store_dword v[54:55], v50, off offset:512
	global_store_dword v[54:55], v46, off offset:768
	v_lshl_add_u64 v[36:37], v[36:37], 0, s[4:5]
	s_and_b64 vcc, exec, s[2:3]
	v_mov_b32_e32 v56, v0
	v_mov_b32_e32 v57, v1
	v_mov_b32_e32 v54, v2
	v_mov_b32_e32 v55, v3
	v_mov_b32_e32 v52, v4
	v_mov_b32_e32 v53, v5
	v_mov_b32_e32 v50, v6
	v_mov_b32_e32 v51, v7
	v_mov_b32_e32 v48, v12
	v_mov_b32_e32 v49, v13
	v_mov_b32_e32 v46, v14
	v_mov_b32_e32 v47, v15
	v_mov_b32_e32 v44, v28
	v_mov_b32_e32 v45, v29
	v_mov_b32_e32 v42, v30
	v_mov_b32_e32 v43, v31
	s_cbranch_vccnz .LBB0_63
.LBB0_61:
	s_cmpk_gt_i32 s6, 0x77ff
	s_cselect_b64 s[2:3], -1, 0
	s_and_b64 vcc, exec, s[2:3]
	s_cbranch_vccnz .LBB0_60
	global_load_dwordx4 v[0:3], v[40:41], off
	global_load_dwordx4 v[4:7], v[40:41], off offset:1024
	global_load_dwordx4 v[12:15], v[40:41], off offset:2048
	global_load_dwordx4 v[28:31], v[40:41], off offset:3072
	s_branch .LBB0_60

.LBB0_1159:
	v_mov_b32_e32 v6, s38
	v_mov_b32_e32 v7, s39
	ds_read_b32 v6, v6
	ds_read_b32 v7, v7
	v_mov_b32_e32 v13, s42
	v_readlane_b32 s11, v255, 5
	s_mov_b64 s[40:41], -1
	s_waitcnt lgkmcnt(1)
	v_readfirstlane_b32 s2, v6
	s_waitcnt lgkmcnt(0)
	v_readfirstlane_b32 s3, v7
	ds_read_b32 v6, v13
	v_mov_b32_e32 v7, s43
	ds_read_b32 v7, v7
	s_cmpk_gt_i32 s10, 0xdff
	v_lshlrev_b32_e32 v160, 2, v0
	s_waitcnt lgkmcnt(1)
	v_readfirstlane_b32 s22, v6
	v_mov_b32_e32 v6, s11
	v_readlane_b32 s11, v255, 6
	s_waitcnt lgkmcnt(0)
	v_readfirstlane_b32 s23, v7
	ds_read_b32 v6, v6
	v_mov_b32_e32 v7, s11
	ds_read_b32 v7, v7
	v_add_u32_e32 v13, 0x420, v12
	v_add_u32_e32 v14, 0x428, v12
	s_waitcnt lgkmcnt(1)
	v_readfirstlane_b32 s36, v6
	v_add_u32_e32 v15, 0x840, v12
	s_waitcnt lgkmcnt(0)
	v_readfirstlane_b32 s37, v7
	v_add_u32_e32 v17, 0x848, v12
	v_add_u32_e32 v18, 0xc60, v12
	v_add_u32_e32 v19, 0xc68, v12
	v_add_u32_e32 v20, 0x1080, v12
	v_add_u32_e32 v21, 0x1088, v12
	v_add_u32_e32 v22, 0x14a0, v12
	v_add_u32_e32 v23, 0x14a8, v12
	v_add_u32_e32 v24, 0x18c0, v12
	v_add_u32_e32 v25, 0x18c8, v12
	v_add_u32_e32 v26, 0x1ce0, v12
	v_add_u32_e32 v27, 0x1ce8, v12
	s_cbranch_scc0 .LBB0_1161
	s_and_b32 s11, s6, 0x7fffffc0
	s_add_i32 s96, s11, 0xffffe400
	s_and_b32 s11, s7, 0x3e0
	s_lshl_b32 s19, s11, 2
	v_add_u32_e32 v6, s96, v1
	s_add_u32 s36, s36, s19
	s_addc_u32 s37, s37, 0
	v_ashrrev_i32_e32 v7, 31, v6
	v_lshl_add_u64 v[28:29], s[36:37], 0, v[160:161]
	v_lshlrev_b64 v[6:7], 12, v[6:7]
	v_lshl_add_u64 v[6:7], v[28:29], 0, v[6:7]
	s_mov_b32 s19, 0x8000
	global_load_dwordx4 v[28:31], v[6:7], off nt
	v_add_co_u32_e32 v32, vcc, s19, v6
	s_mov_b32 s19, 0x10000
	s_nop 0
	v_addc_co_u32_e32 v33, vcc, 0, v7, vcc
	global_load_dwordx4 v[32:35], v[32:33], off nt
	v_add_co_u32_e32 v36, vcc, s19, v6
	s_mov_b32 s19, 0x18000
	s_nop 0
	v_addc_co_u32_e32 v37, vcc, 0, v7, vcc
	global_load_dwordx4 v[36:39], v[36:37], off nt
	v_add_co_u32_e32 v40, vcc, s19, v6
	s_mov_b32 s19, 0x20000
	s_nop 0
	v_addc_co_u32_e32 v41, vcc, 0, v7, vcc
	global_load_dwordx4 v[40:43], v[40:41], off nt
	v_add_co_u32_e32 v44, vcc, s19, v6
	s_mov_b32 s19, 0x28000
	s_nop 0
	v_addc_co_u32_e32 v45, vcc, 0, v7, vcc
	global_load_dwordx4 v[44:47], v[44:45], off nt
	v_add_co_u32_e32 v48, vcc, s19, v6
	s_mov_b32 s19, 0x30000
	s_nop 0
	v_addc_co_u32_e32 v49, vcc, 0, v7, vcc
	global_load_dwordx4 v[48:51], v[48:49], off nt
	v_add_co_u32_e32 v52, vcc, s19, v6
	s_mov_b32 s19, 0x38000
	s_nop 0
	v_addc_co_u32_e32 v53, vcc, 0, v7, vcc
	global_load_dwordx4 v[52:55], v[52:53], off nt
	v_add_co_u32_e32 v6, vcc, s19, v6
	s_movk_i32 s19, 0x1c00
	s_nop 0
	v_addc_co_u32_e32 v7, vcc, 0, v7, vcc
	global_load_dwordx4 v[56:59], v[6:7], off nt
	v_lshl_add_u64 v[6:7], s[96:97], 1, v[2:3]
	s_mov_b64 s[40:41], 0
	s_waitcnt vmcnt(7)
	ds_write2_b32 v12, v28, v29 offset1:1
	ds_write2_b32 v12, v30, v31 offset0:2 offset1:3
	s_waitcnt vmcnt(6)
	ds_write2_b32 v13, v32, v33 offset1:1
	ds_write2_b32 v14, v34, v35 offset1:1
	s_waitcnt vmcnt(5)
	ds_write2_b32 v15, v36, v37 offset1:1
	ds_write2_b32 v17, v38, v39 offset1:1
	s_waitcnt vmcnt(4)
	ds_write2_b32 v18, v40, v41 offset1:1
	ds_write2_b32 v19, v42, v43 offset1:1
	s_waitcnt vmcnt(3)
	ds_write2_b32 v20, v44, v45 offset1:1
	ds_write2_b32 v21, v46, v47 offset1:1
	s_waitcnt vmcnt(2)
	ds_write2_b32 v22, v48, v49 offset1:1
	ds_write2_b32 v23, v50, v51 offset1:1
	s_waitcnt vmcnt(1)
	ds_write2_b32 v24, v52, v53 offset1:1
	ds_write2_b32 v25, v54, v55 offset1:1
	s_waitcnt vmcnt(0)
	ds_write2_b32 v26, v56, v57 offset1:1
	ds_write2_b32 v27, v58, v59 offset1:1
	s_waitcnt lgkmcnt(0)
	ds_read2_b32 v[32:33], v11 offset0:33 offset1:41
	ds_read2_b32 v[34:35], v11 offset1:8
	ds_read2_b32 v[36:37], v11 offset0:66 offset1:74
	ds_read2_b32 v[38:39], v11 offset0:99 offset1:107
	ds_read2_b32 v[40:41], v11 offset0:132 offset1:140
	ds_read2_b32 v[42:43], v11 offset0:165 offset1:173
	ds_read2_b32 v[44:45], v11 offset0:198 offset1:206
	ds_read2_b32 v[46:47], v11 offset0:231 offset1:239
	s_waitcnt lgkmcnt(6)
	v_cvt_pk_bf16_f32 v28, v34, v32
	v_add_u32_e32 v32, s11, v1
	s_waitcnt lgkmcnt(4)
	v_cvt_pk_bf16_f32 v29, v36, v38
	s_waitcnt lgkmcnt(2)
	v_cvt_pk_bf16_f32 v30, v40, v42
	s_waitcnt lgkmcnt(0)
	v_cvt_pk_bf16_f32 v31, v44, v46
	v_mad_i64_i32 v[48:49], s[36:37], v32, s19, v[6:7]
	v_add_u32_e32 v32, s11, v8
	global_store_dwordx4 v[48:49], v[28:31], off
	s_nop 1
	v_cvt_pk_bf16_f32 v28, v35, v33
	v_cvt_pk_bf16_f32 v29, v37, v39
	v_cvt_pk_bf16_f32 v30, v41, v43
	v_cvt_pk_bf16_f32 v31, v45, v47
	v_mad_i64_i32 v[32:33], s[36:37], v32, s19, v[6:7]
	global_store_dwordx4 v[32:33], v[28:31], off
	ds_read2_b32 v[32:33], v11 offset0:49 offset1:57
	ds_read2_b32 v[34:35], v11 offset0:16 offset1:24
	ds_read2_b32 v[36:37], v11 offset0:82 offset1:90
	ds_read2_b32 v[38:39], v11 offset0:115 offset1:123
	ds_read2_b32 v[40:41], v11 offset0:148 offset1:156
	ds_read2_b32 v[42:43], v11 offset0:181 offset1:189
	ds_read2_b32 v[44:45], v11 offset0:214 offset1:222
	ds_read2_b32 v[46:47], v11 offset0:247 offset1:255
	s_waitcnt lgkmcnt(6)
	v_cvt_pk_bf16_f32 v28, v34, v32
	v_add_u32_e32 v32, s11, v9
	s_waitcnt lgkmcnt(4)
	v_cvt_pk_bf16_f32 v29, v36, v38
	s_waitcnt lgkmcnt(2)
	v_cvt_pk_bf16_f32 v30, v40, v42
	s_waitcnt lgkmcnt(0)
	v_cvt_pk_bf16_f32 v31, v44, v46
	v_mad_i64_i32 v[48:49], s[36:37], v32, s19, v[6:7]
	v_add_u32_e32 v32, s11, v10
	global_store_dwordx4 v[48:49], v[28:31], off
	v_mad_i64_i32 v[6:7], s[36:37], v32, s19, v[6:7]
	s_nop 0
	v_cvt_pk_bf16_f32 v28, v35, v33
	v_cvt_pk_bf16_f32 v29, v37, v39
	v_cvt_pk_bf16_f32 v30, v41, v43
	v_cvt_pk_bf16_f32 v31, v45, v47
	global_store_dwordx4 v[6:7], v[28:31], off
	s_waitcnt lgkmcnt(0)
.LBB0_1161:
	s_andn2_b64 vcc, exec, s[40:41]
	s_cbranch_vccnz .LBB0_1158
	s_mul_hi_i32 s11, s10, 0x92492493
	s_add_i32 s11, s11, s10
	s_lshr_b32 s19, s11, 31
	s_ashr_i32 s11, s11, 10
	s_add_i32 s11, s11, s19
	s_mul_i32 s19, s11, 0xfffff900
	s_add_i32 s19, s10, s19
	s_mul_i32 s31, s19, 0x4925
	s_lshr_b32 s33, s31, 31
	s_ashr_i32 s31, s31, 21
	s_add_i32 s31, s31, s33
	s_sext_i32_i16 s33, s31
	s_mulk_i32 s31, 0x70
	s_sub_i32 s19, s19, s31
	s_add_i32 s31, s10, 0x6ff
	s_sext_i32_i16 s19, s19
	s_cmpk_lt_u32 s31, 0xdff
	s_cselect_b32 s3, s3, s23
	s_cselect_b32 s23, s2, s22
	s_lshl_b32 s36, s19, 5
	s_lshl_b32 s2, s19, 6
	s_and_b32 s2, s2, 0xffffff00
	s_and_b32 s19, s36, 0x60
	s_or_b32 s2, s2, s19
	s_lshl_b32 s11, s11, 7
	s_ashr_i32 s37, s36, 31
	s_lshl_b32 s22, s33, 6
	s_add_i32 s2, s2, s11
	s_lshl_b64 s[36:37], s[36:37], 2
	s_add_u32 s36, s23, s36
	s_addc_u32 s37, s3, s37
	v_add_u32_e32 v56, s22, v1
	v_lshl_add_u64 v[6:7], s[36:37], 0, v[160:161]
	s_movk_i32 s3, 0x3800
	v_mad_i64_i32 v[28:29], s[36:37], v56, s3, v[6:7]
	global_load_dwordx4 v[28:31], v[28:29], off nt
	v_add_u32_e32 v32, 8, v56
	v_mad_i64_i32 v[32:33], s[36:37], v32, s3, v[6:7]
	global_load_dwordx4 v[32:35], v[32:33], off nt
	v_add_u32_e32 v36, 16, v56
	v_mad_i64_i32 v[36:37], s[36:37], v36, s3, v[6:7]
	global_load_dwordx4 v[36:39], v[36:37], off nt
	v_add_u32_e32 v40, 24, v56
	v_mad_i64_i32 v[40:41], s[36:37], v40, s3, v[6:7]
	global_load_dwordx4 v[40:43], v[40:41], off nt
	v_add_u32_e32 v44, 32, v56
	v_mad_i64_i32 v[44:45], s[36:37], v44, s3, v[6:7]
	global_load_dwordx4 v[44:47], v[44:45], off nt
	v_add_u32_e32 v48, 40, v56
	v_mad_i64_i32 v[48:49], s[36:37], v48, s3, v[6:7]
	global_load_dwordx4 v[48:51], v[48:49], off nt
	v_add_u32_e32 v52, 48, v56
	v_mad_i64_i32 v[52:53], s[36:37], v52, s3, v[6:7]
	global_load_dwordx4 v[52:55], v[52:53], off nt
	v_add_u32_e32 v56, 56, v56
	v_mad_i64_i32 v[6:7], s[36:37], v56, s3, v[6:7]
	global_load_dwordx4 v[56:59], v[6:7], off nt
	s_ashr_i32 s23, s22, 31
	v_lshl_add_u64 v[6:7], s[22:23], 1, v[4:5]
	s_waitcnt vmcnt(7)
	ds_write2_b32 v12, v28, v29 offset1:1
	ds_write2_b32 v12, v30, v31 offset0:2 offset1:3
	s_waitcnt vmcnt(6)
	ds_write2_b32 v13, v32, v33 offset1:1
	ds_write2_b32 v14, v34, v35 offset1:1
	s_waitcnt vmcnt(5)
	ds_write2_b32 v15, v36, v37 offset1:1
	ds_write2_b32 v17, v38, v39 offset1:1
	s_waitcnt vmcnt(4)
	ds_write2_b32 v18, v40, v41 offset1:1
	ds_write2_b32 v19, v42, v43 offset1:1
	s_waitcnt vmcnt(3)
	ds_write2_b32 v20, v44, v45 offset1:1
	ds_write2_b32 v21, v46, v47 offset1:1
	s_waitcnt vmcnt(2)
	ds_write2_b32 v22, v48, v49 offset1:1
	ds_write2_b32 v23, v50, v51 offset1:1
	s_waitcnt vmcnt(1)
	ds_write2_b32 v24, v52, v53 offset1:1
	ds_write2_b32 v25, v54, v55 offset1:1
	s_waitcnt vmcnt(0)
	ds_write2_b32 v26, v56, v57 offset1:1
	ds_write2_b32 v27, v58, v59 offset1:1
	s_waitcnt lgkmcnt(0)
	ds_read2_b32 v[14:15], v11 offset0:33 offset1:41
	ds_read2_b32 v[22:23], v11 offset1:8
	ds_read2_b32 v[24:25], v11 offset0:66 offset1:74
	ds_read2_b32 v[26:27], v11 offset0:99 offset1:107
	ds_read2_b32 v[28:29], v11 offset0:132 offset1:140
	ds_read2_b32 v[30:31], v11 offset0:165 offset1:173
	ds_read2_b32 v[32:33], v11 offset0:198 offset1:206
	ds_read2_b32 v[34:35], v11 offset0:231 offset1:239
	v_add_u32_e32 v36, s2, v1
	v_ashrrev_i32_e32 v37, 31, v36
	v_lshlrev_b64 v[36:37], 11, v[36:37]
	s_waitcnt lgkmcnt(6)
	v_cvt_pk_bf16_f32 v18, v22, v14
	s_waitcnt lgkmcnt(4)
	v_cvt_pk_bf16_f32 v19, v24, v26
	s_waitcnt lgkmcnt(2)
	v_cvt_pk_bf16_f32 v20, v28, v30
	s_waitcnt lgkmcnt(0)
	v_cvt_pk_bf16_f32 v21, v32, v34
	v_lshl_add_u64 v[36:37], v[6:7], 0, v[36:37]
	v_add_u32_e32 v14, s2, v8
	global_store_dwordx4 v[36:37], v[18:21], off
	v_add_u32_e32 v36, s2, v9
	v_ashrrev_i32_e32 v37, 31, v36
	v_cvt_pk_bf16_f32 v18, v23, v15
	v_ashrrev_i32_e32 v15, 31, v14
	v_lshlrev_b64 v[14:15], 11, v[14:15]
	v_cvt_pk_bf16_f32 v19, v25, v27
	v_cvt_pk_bf16_f32 v20, v29, v31
	v_cvt_pk_bf16_f32 v21, v33, v35
	v_lshl_add_u64 v[14:15], v[6:7], 0, v[14:15]
	global_store_dwordx4 v[14:15], v[18:21], off
	ds_read2_b32 v[14:15], v11 offset0:49 offset1:57
	ds_read2_b32 v[22:23], v11 offset0:16 offset1:24
	ds_read2_b32 v[24:25], v11 offset0:82 offset1:90
	ds_read2_b32 v[26:27], v11 offset0:115 offset1:123
	ds_read2_b32 v[28:29], v11 offset0:148 offset1:156
	ds_read2_b32 v[30:31], v11 offset0:181 offset1:189
	ds_read2_b32 v[32:33], v11 offset0:214 offset1:222
	ds_read2_b32 v[34:35], v11 offset0:247 offset1:255
	v_lshlrev_b64 v[36:37], 11, v[36:37]
	s_waitcnt lgkmcnt(6)
	v_cvt_pk_bf16_f32 v18, v22, v14
	s_waitcnt lgkmcnt(4)
	v_cvt_pk_bf16_f32 v19, v24, v26
	s_waitcnt lgkmcnt(2)
	v_cvt_pk_bf16_f32 v20, v28, v30
	s_waitcnt lgkmcnt(0)
	v_cvt_pk_bf16_f32 v21, v32, v34
	v_lshl_add_u64 v[36:37], v[6:7], 0, v[36:37]
	v_add_u32_e32 v14, s2, v10
	global_store_dwordx4 v[36:37], v[18:21], off
	s_nop 1
	v_cvt_pk_bf16_f32 v18, v23, v15
	v_ashrrev_i32_e32 v15, 31, v14
	v_lshlrev_b64 v[14:15], 11, v[14:15]
	v_cvt_pk_bf16_f32 v19, v25, v27
	v_cvt_pk_bf16_f32 v20, v29, v31
	v_cvt_pk_bf16_f32 v21, v33, v35
	v_lshl_add_u64 v[6:7], v[6:7], 0, v[14:15]
	global_store_dwordx4 v[6:7], v[18:21], off
	s_waitcnt lgkmcnt(0)
	s_branch .LBB0_1158

.LBB0_1377:
	v_readlane_b32 s3, v255, 9
	s_mul_hi_i32 s2, s38, 0x30c30c31
	s_ashr_i32 s44, s2, 10
	v_mov_b32_e32 v4, s3
	v_readlane_b32 s3, v255, 10
	ds_read_b32 v4, v4
	s_mov_b64 s[22:23], -1
	v_mov_b32_e32 v5, s3
	ds_read_b32 v5, v5
	s_lshr_b32 s3, s2, 31
	v_readlane_b32 s2, v255, 11
	s_waitcnt lgkmcnt(1)
	v_readfirstlane_b32 s18, v4
	s_add_i32 s44, s44, s3
	s_waitcnt lgkmcnt(0)
	v_readfirstlane_b32 s19, v5
	v_mov_b32_e32 v4, s2
	v_readlane_b32 s2, v255, 12
	ds_read_b32 v4, v4
	s_mul_i32 s3, s44, 0xa80000
	v_mov_b32_e32 v5, s2
	ds_read_b32 v5, v5
	s_add_u32 s39, s10, s3
	v_readlane_b32 s3, v255, 13
	s_waitcnt lgkmcnt(1)
	v_readfirstlane_b32 s36, v4
	s_mul_hi_i32 s2, s44, 0xa80000
	v_mov_b32_e32 v4, s3
	v_readlane_b32 s3, v255, 14
	s_waitcnt lgkmcnt(0)
	v_readfirstlane_b32 s37, v5
	ds_read_b32 v4, v4
	v_mov_b32_e32 v5, s3
	ds_read_b32 v5, v5
	s_addc_u32 s40, s11, s2
	s_mul_i32 s2, s44, 0xffffeb00
	s_add_i32 s41, s38, s2
	s_waitcnt lgkmcnt(1)
	v_readfirstlane_b32 s2, v4
	s_waitcnt lgkmcnt(0)
	v_readfirstlane_b32 s3, v5
	s_cmpk_gt_i32 s41, 0xdff
	s_mul_hi_i32 s42, s44, 0xe00000
	s_mul_i32 s43, s44, 0xe00000
	v_lshlrev_b32_e32 v160, 2, v0
	v_add_u32_e32 v37, 0x420, v23
	v_add_u32_e32 v36, 0x428, v23
	v_add_u32_e32 v35, 0x840, v23
	v_add_u32_e32 v34, 0x848, v23
	v_add_u32_e32 v33, 0xc60, v23
	v_add_u32_e32 v32, 0xc68, v23
	v_add_u32_e32 v31, 0x1080, v23
	v_add_u32_e32 v30, 0x1088, v23
	v_add_u32_e32 v29, 0x14a0, v23
	v_add_u32_e32 v28, 0x14a8, v23
	v_add_u32_e32 v27, 0x18c0, v23
	v_add_u32_e32 v26, 0x18c8, v23
	v_add_u32_e32 v25, 0x1ce0, v23
	v_add_u32_e32 v24, 0x1ce8, v23
	s_cbranch_scc0 .LBB0_1379
	s_add_u32 s22, s2, s43
	s_mulk_i32 s44, 0xd600
	s_addc_u32 s3, s3, s42
	s_add_i32 s2, s33, s44
	s_and_b32 s2, s2, 0x7fffffc0
	s_add_i32 s44, s2, 0xffffe400
	s_and_b32 s2, s31, 0x3e0
	s_lshl_b32 s23, s2, 2
	v_add_u32_e32 v4, s44, v1
	s_add_u32 s22, s22, s23
	s_addc_u32 s23, s3, 0
	v_ashrrev_i32_e32 v5, 31, v4
	v_lshl_add_u64 v[6:7], s[22:23], 0, v[160:161]
	v_lshlrev_b64 v[4:5], 12, v[4:5]
	v_lshl_add_u64 v[18:19], v[6:7], 0, v[4:5]
	s_mov_b32 s3, 0x8000
	global_load_dwordx4 v[4:7], v[18:19], off nt
	v_add_co_u32_e32 v10, vcc, s3, v18
	s_mov_b32 s3, 0x10000
	s_nop 0
	v_addc_co_u32_e32 v11, vcc, 0, v19, vcc
	global_load_dwordx4 v[10:13], v[10:11], off nt
	v_add_co_u32_e32 v14, vcc, s3, v18
	s_mov_b32 s3, 0x18000
	s_nop 0
	v_addc_co_u32_e32 v15, vcc, 0, v19, vcc
	global_load_dwordx4 v[14:17], v[14:15], off nt
	v_add_co_u32_e32 v38, vcc, s3, v18
	s_mov_b32 s3, 0x20000
	s_nop 0
	v_addc_co_u32_e32 v39, vcc, 0, v19, vcc
	global_load_dwordx4 v[38:41], v[38:39], off nt
	v_add_co_u32_e32 v42, vcc, s3, v18
	s_mov_b32 s3, 0x28000
	s_nop 0
	v_addc_co_u32_e32 v43, vcc, 0, v19, vcc
	global_load_dwordx4 v[42:45], v[42:43], off nt
	v_add_co_u32_e32 v46, vcc, s3, v18
	s_mov_b32 s3, 0x30000
	s_nop 0
	v_addc_co_u32_e32 v47, vcc, 0, v19, vcc
	global_load_dwordx4 v[46:49], v[46:47], off nt
	v_add_co_u32_e32 v50, vcc, s3, v18
	s_mov_b32 s3, 0x38000
	s_nop 0
	v_addc_co_u32_e32 v51, vcc, 0, v19, vcc
	global_load_dwordx4 v[50:53], v[50:51], off nt
	v_add_co_u32_e32 v18, vcc, s3, v18
	s_mov_b32 s4, 0x42800000
	s_nop 0
	v_addc_co_u32_e32 v19, vcc, 0, v19, vcc
	global_load_dwordx4 v[54:57], v[18:19], off nt
	s_add_u32 s22, s39, s44
	s_addc_u32 s23, s40, 0
	s_movk_i32 s3, 0xe00
	s_waitcnt vmcnt(7)
	v_pk_mul_f32 v[4:5], v[4:5], s[4:5] op_sel_hi:[1,0]
	ds_write2_b32 v23, v4, v5 offset1:1
	v_pk_mul_f32 v[4:5], v[6:7], s[4:5] op_sel_hi:[1,0]
	ds_write2_b32 v23, v4, v5 offset0:2 offset1:3
	s_waitcnt vmcnt(6)
	v_pk_mul_f32 v[4:5], v[10:11], s[4:5] op_sel_hi:[1,0]
	ds_write2_b32 v37, v4, v5 offset1:1
	v_pk_mul_f32 v[4:5], v[12:13], s[4:5] op_sel_hi:[1,0]
	ds_write2_b32 v36, v4, v5 offset1:1
	s_waitcnt vmcnt(5)
	v_pk_mul_f32 v[4:5], v[14:15], s[4:5] op_sel_hi:[1,0]
	ds_write2_b32 v35, v4, v5 offset1:1
	v_pk_mul_f32 v[4:5], v[16:17], s[4:5] op_sel_hi:[1,0]
	ds_write2_b32 v34, v4, v5 offset1:1
	s_waitcnt vmcnt(4)
	v_pk_mul_f32 v[4:5], v[38:39], s[4:5] op_sel_hi:[1,0]
	ds_write2_b32 v33, v4, v5 offset1:1
	v_pk_mul_f32 v[4:5], v[40:41], s[4:5] op_sel_hi:[1,0]
	ds_write2_b32 v32, v4, v5 offset1:1
	v_mov_b32_e32 v38, v161
	v_mov_b32_e32 v39, v161
	s_waitcnt vmcnt(3)
	v_pk_mul_f32 v[4:5], v[42:43], s[4:5] op_sel_hi:[1,0]
	ds_write2_b32 v31, v4, v5 offset1:1
	v_pk_mul_f32 v[4:5], v[44:45], s[4:5] op_sel_hi:[1,0]
	ds_write2_b32 v30, v4, v5 offset1:1
	s_waitcnt vmcnt(2)
	v_pk_mul_f32 v[4:5], v[46:47], s[4:5] op_sel_hi:[1,0]
	ds_write2_b32 v29, v4, v5 offset1:1
	v_pk_mul_f32 v[4:5], v[48:49], s[4:5] op_sel_hi:[1,0]
	ds_write2_b32 v28, v4, v5 offset1:1
	s_waitcnt vmcnt(1)
	v_pk_mul_f32 v[4:5], v[50:51], s[4:5] op_sel_hi:[1,0]
	ds_write2_b32 v27, v4, v5 offset1:1
	v_pk_mul_f32 v[4:5], v[52:53], s[4:5] op_sel_hi:[1,0]
	ds_write2_b32 v26, v4, v5 offset1:1
	s_waitcnt vmcnt(0)
	v_pk_mul_f32 v[4:5], v[54:55], s[4:5] op_sel_hi:[1,0]
	ds_write2_b32 v25, v4, v5 offset1:1
	v_pk_mul_f32 v[4:5], v[56:57], s[4:5] op_sel_hi:[1,0]
	ds_write2_b32 v24, v4, v5 offset1:1
	s_waitcnt lgkmcnt(0)
	ds_read2_b32 v[6:7], v22 offset0:33 offset1:41
	ds_read2_b32 v[10:11], v22 offset0:66 offset1:74
	ds_read2_b32 v[12:13], v22 offset0:99 offset1:107
	ds_read2_b32 v[14:15], v22 offset1:8
	v_lshl_add_u64 v[4:5], s[22:23], 0, v[2:3]
	s_mov_b64 s[4:5], 0x700000
	v_lshl_add_u64 v[4:5], v[4:5], 0, s[4:5]
	ds_read2_b32 v[40:41], v22 offset0:132 offset1:140
	ds_read2_b32 v[42:43], v22 offset0:165 offset1:173
	ds_read2_b32 v[16:17], v22 offset0:198 offset1:206
	ds_read2_b32 v[18:19], v22 offset0:231 offset1:239
	s_waitcnt lgkmcnt(4)
	v_cvt_pk_fp8_f32 v38, v14, v6
	v_add_u32_e32 v6, s2, v1
	v_mad_i64_i32 v[44:45], s[22:23], v6, s3, v[4:5]
	v_mov_b32_e32 v6, v161
	v_cvt_pk_fp8_f32 v6, v15, v7
	v_mov_b32_e32 v7, v161
	s_waitcnt lgkmcnt(2)
	v_cvt_pk_fp8_f32 v39, v40, v42
	v_cvt_pk_fp8_f32 v7, v41, v43
	v_cvt_pk_fp8_f32 v38, v10, v12 op_sel:[0,0,1]
	v_cvt_pk_fp8_f32 v6, v11, v13 op_sel:[0,0,1]
	s_waitcnt lgkmcnt(0)
	v_cvt_pk_fp8_f32 v39, v16, v18 op_sel:[0,0,1]
	v_cvt_pk_fp8_f32 v7, v17, v19 op_sel:[0,0,1]
	v_add_u32_e32 v10, s2, v9
	v_mad_i64_i32 v[10:11], s[22:23], v10, s3, v[4:5]
	global_store_dwordx2 v[44:45], v[38:39], off
	global_store_dwordx2 v[10:11], v[6:7], off
	ds_read2_b32 v[6:7], v22 offset0:49 offset1:57
	ds_read2_b32 v[10:11], v22 offset0:82 offset1:90
	ds_read2_b32 v[12:13], v22 offset0:115 offset1:123
	ds_read2_b32 v[14:15], v22 offset0:16 offset1:24
	v_mov_b32_e32 v16, v161
	ds_read2_b32 v[18:19], v22 offset0:148 offset1:156
	ds_read2_b32 v[38:39], v22 offset0:181 offset1:189
	ds_read2_b32 v[40:41], v22 offset0:214 offset1:222
	ds_read2_b32 v[42:43], v22 offset0:247 offset1:255
	v_mov_b32_e32 v17, v161
	s_waitcnt lgkmcnt(4)
	v_cvt_pk_fp8_f32 v16, v14, v6
	v_add_u32_e32 v6, s2, v20
	v_mad_i64_i32 v[44:45], s[22:23], v6, s3, v[4:5]
	v_mov_b32_e32 v6, v161
	v_cvt_pk_fp8_f32 v6, v15, v7
	v_mov_b32_e32 v7, v161
	s_waitcnt lgkmcnt(2)
	v_cvt_pk_fp8_f32 v17, v18, v38
	v_cvt_pk_fp8_f32 v7, v19, v39
	v_cvt_pk_fp8_f32 v16, v10, v12 op_sel:[0,0,1]
	v_cvt_pk_fp8_f32 v6, v11, v13 op_sel:[0,0,1]
	s_waitcnt lgkmcnt(0)
	v_cvt_pk_fp8_f32 v17, v40, v42 op_sel:[0,0,1]
	v_cvt_pk_fp8_f32 v7, v41, v43 op_sel:[0,0,1]
	v_add_u32_e32 v10, s2, v21
	v_mad_i64_i32 v[4:5], s[2:3], v10, s3, v[4:5]
	global_store_dwordx2 v[44:45], v[16:17], off
	global_store_dwordx2 v[4:5], v[6:7], off
	s_waitcnt lgkmcnt(0)
	s_mov_b64 s[22:23], 0
.LBB0_1379:
	s_andn2_b64 vcc, exec, s[22:23]
	s_cbranch_vccnz .LBB0_1376
	s_mul_i32 s2, s41, 0x4925
	s_lshr_b32 s3, s2, 31
	s_ashr_i32 s2, s2, 25
	s_add_i32 s2, s2, s3
	s_sext_i32_i16 s3, s2
	s_mulk_i32 s2, 0x700
	s_sub_i32 s2, s41, s2
	s_sext_i32_i16 s22, s2
	s_mulk_i32 s22, 0x4925
	s_lshr_b32 s23, s22, 31
	s_ashr_i32 s22, s22, 21
	s_add_i32 s22, s22, s23
	s_sext_i32_i16 s23, s22
	s_mulk_i32 s22, 0x70
	s_sub_i32 s2, s2, s22
	s_addk_i32 s41, 0x6ff
	s_cmpk_lt_u32 s41, 0xdff
	s_cselect_b32 s18, s18, s36
	s_sext_i32_i16 s2, s2
	s_cselect_b32 s19, s19, s37
	s_add_u32 s22, s18, s43
	s_addc_u32 s36, s19, s42
	s_lshl_b32 s18, s2, 5
	s_lshl_b32 s2, s2, 6
	s_and_b32 s2, s2, 0xffffff00
	s_and_b32 s19, s18, 0x60
	s_or_b32 s2, s2, s19
	s_lshl_b32 s3, s3, 7
	s_ashr_i32 s19, s18, 31
	s_lshl_b32 s23, s23, 6
	s_add_i32 s2, s2, s3
	s_lshl_b64 s[18:19], s[18:19], 2
	s_add_u32 s18, s22, s18
	s_addc_u32 s19, s36, s19
	v_add_u32_e32 v54, s23, v1
	v_lshl_add_u64 v[18:19], s[18:19], 0, v[160:161]
	s_movk_i32 s3, 0x3800
	v_mad_i64_i32 v[4:5], s[18:19], v54, s3, v[18:19]
	global_load_dwordx4 v[4:7], v[4:5], off nt
	v_add_u32_e32 v10, 8, v54
	v_mad_i64_i32 v[10:11], s[18:19], v10, s3, v[18:19]
	global_load_dwordx4 v[10:13], v[10:11], off nt
	v_add_u32_e32 v14, 16, v54
	v_mad_i64_i32 v[14:15], s[18:19], v14, s3, v[18:19]
	global_load_dwordx4 v[14:17], v[14:15], off nt
	v_add_u32_e32 v38, 24, v54
	v_mad_i64_i32 v[38:39], s[18:19], v38, s3, v[18:19]
	global_load_dwordx4 v[38:41], v[38:39], off nt
	v_add_u32_e32 v42, 32, v54
	v_mad_i64_i32 v[42:43], s[18:19], v42, s3, v[18:19]
	global_load_dwordx4 v[42:45], v[42:43], off nt
	v_add_u32_e32 v46, 40, v54
	v_mad_i64_i32 v[46:47], s[18:19], v46, s3, v[18:19]
	global_load_dwordx4 v[46:49], v[46:47], off nt
	v_add_u32_e32 v50, 48, v54
	v_mad_i64_i32 v[50:51], s[18:19], v50, s3, v[18:19]
	global_load_dwordx4 v[50:53], v[50:51], off nt
	v_add_u32_e32 v54, 56, v54
	v_mad_i64_i32 v[18:19], s[18:19], v54, s3, v[18:19]
	global_load_dwordx4 v[54:57], v[18:19], off nt
	s_mov_b32 s4, 0x42000000
	s_ashr_i32 s3, s23, 31
	s_add_u32 s18, s39, s23
	s_addc_u32 s19, s40, s3
	s_waitcnt vmcnt(7)
	v_pk_mul_f32 v[4:5], v[4:5], s[4:5] op_sel_hi:[1,0]
	ds_write2_b32 v23, v4, v5 offset1:1
	v_pk_mul_f32 v[4:5], v[6:7], s[4:5] op_sel_hi:[1,0]
	ds_write2_b32 v23, v4, v5 offset0:2 offset1:3
	s_waitcnt vmcnt(6)
	v_pk_mul_f32 v[4:5], v[10:11], s[4:5] op_sel_hi:[1,0]
	ds_write2_b32 v37, v4, v5 offset1:1
	v_pk_mul_f32 v[4:5], v[12:13], s[4:5] op_sel_hi:[1,0]
	ds_write2_b32 v36, v4, v5 offset1:1
	s_waitcnt vmcnt(5)
	v_pk_mul_f32 v[4:5], v[14:15], s[4:5] op_sel_hi:[1,0]
	ds_write2_b32 v35, v4, v5 offset1:1
	v_pk_mul_f32 v[4:5], v[16:17], s[4:5] op_sel_hi:[1,0]
	ds_write2_b32 v34, v4, v5 offset1:1
	s_waitcnt vmcnt(4)
	v_pk_mul_f32 v[4:5], v[38:39], s[4:5] op_sel_hi:[1,0]
	ds_write2_b32 v33, v4, v5 offset1:1
	v_pk_mul_f32 v[4:5], v[40:41], s[4:5] op_sel_hi:[1,0]
	ds_write2_b32 v32, v4, v5 offset1:1
	s_waitcnt vmcnt(3)
	v_pk_mul_f32 v[4:5], v[42:43], s[4:5] op_sel_hi:[1,0]
	ds_write2_b32 v31, v4, v5 offset1:1
	v_pk_mul_f32 v[4:5], v[44:45], s[4:5] op_sel_hi:[1,0]
	ds_write2_b32 v30, v4, v5 offset1:1
	s_waitcnt vmcnt(2)
	v_pk_mul_f32 v[4:5], v[46:47], s[4:5] op_sel_hi:[1,0]
	ds_write2_b32 v29, v4, v5 offset1:1
	v_pk_mul_f32 v[4:5], v[48:49], s[4:5] op_sel_hi:[1,0]
	ds_write2_b32 v28, v4, v5 offset1:1
	s_waitcnt vmcnt(1)
	v_pk_mul_f32 v[4:5], v[50:51], s[4:5] op_sel_hi:[1,0]
	ds_write2_b32 v27, v4, v5 offset1:1
	v_pk_mul_f32 v[4:5], v[52:53], s[4:5] op_sel_hi:[1,0]
	ds_write2_b32 v26, v4, v5 offset1:1
	s_waitcnt vmcnt(0)
	v_pk_mul_f32 v[4:5], v[54:55], s[4:5] op_sel_hi:[1,0]
	ds_write2_b32 v25, v4, v5 offset1:1
	v_pk_mul_f32 v[4:5], v[56:57], s[4:5] op_sel_hi:[1,0]
	ds_write2_b32 v24, v4, v5 offset1:1
	s_waitcnt lgkmcnt(0)
	ds_read2_b32 v[6:7], v22 offset0:33 offset1:41
	ds_read2_b32 v[10:11], v22 offset0:66 offset1:74
	ds_read2_b32 v[12:13], v22 offset0:99 offset1:107
	ds_read2_b32 v[14:15], v22 offset1:8
	v_mov_b32_e32 v16, v161
	ds_read2_b32 v[18:19], v22 offset0:132 offset1:140
	ds_read2_b32 v[24:25], v22 offset0:165 offset1:173
	ds_read2_b32 v[26:27], v22 offset0:198 offset1:206
	ds_read2_b32 v[28:29], v22 offset0:231 offset1:239
	v_mov_b32_e32 v17, v161
	v_add_u32_e32 v30, s2, v1
	s_waitcnt lgkmcnt(4)
	v_cvt_pk_fp8_f32 v16, v14, v6
	v_mov_b32_e32 v6, v161
	v_cvt_pk_fp8_f32 v6, v15, v7
	v_mov_b32_e32 v7, v161
	s_waitcnt lgkmcnt(2)
	v_cvt_pk_fp8_f32 v17, v18, v24
	v_cvt_pk_fp8_f32 v7, v19, v25
	v_cvt_pk_fp8_f32 v16, v10, v12 op_sel:[0,0,1]
	v_cvt_pk_fp8_f32 v6, v11, v13 op_sel:[0,0,1]
	s_waitcnt lgkmcnt(0)
	v_cvt_pk_fp8_f32 v17, v26, v28 op_sel:[0,0,1]
	v_cvt_pk_fp8_f32 v7, v27, v29 op_sel:[0,0,1]
	v_add_u32_e32 v10, s2, v9
	v_ashrrev_i32_e32 v31, 31, v30
	v_ashrrev_i32_e32 v11, 31, v10
	v_lshl_add_u64 v[4:5], s[18:19], 0, v[2:3]
	v_lshlrev_b64 v[30:31], 10, v[30:31]
	v_lshlrev_b64 v[10:11], 10, v[10:11]
	v_lshl_add_u64 v[30:31], v[4:5], 0, v[30:31]
	v_lshl_add_u64 v[10:11], v[4:5], 0, v[10:11]
	global_store_dwordx2 v[30:31], v[16:17], off
	global_store_dwordx2 v[10:11], v[6:7], off
	ds_read2_b32 v[6:7], v22 offset0:49 offset1:57
	ds_read2_b32 v[10:11], v22 offset0:82 offset1:90
	ds_read2_b32 v[12:13], v22 offset0:115 offset1:123
	ds_read2_b32 v[14:15], v22 offset0:16 offset1:24
	v_mov_b32_e32 v16, v161
	ds_read2_b32 v[18:19], v22 offset0:148 offset1:156
	ds_read2_b32 v[24:25], v22 offset0:181 offset1:189
	ds_read2_b32 v[26:27], v22 offset0:214 offset1:222
	ds_read2_b32 v[28:29], v22 offset0:247 offset1:255
	v_mov_b32_e32 v17, v161
	v_add_u32_e32 v30, s2, v20
	s_waitcnt lgkmcnt(4)
	v_cvt_pk_fp8_f32 v16, v14, v6
	v_mov_b32_e32 v6, v161
	v_cvt_pk_fp8_f32 v6, v15, v7
	v_mov_b32_e32 v7, v161
	s_waitcnt lgkmcnt(2)
	v_cvt_pk_fp8_f32 v17, v18, v24
	v_cvt_pk_fp8_f32 v7, v19, v25
	v_cvt_pk_fp8_f32 v16, v10, v12 op_sel:[0,0,1]
	v_cvt_pk_fp8_f32 v6, v11, v13 op_sel:[0,0,1]
	s_waitcnt lgkmcnt(0)
	v_cvt_pk_fp8_f32 v17, v26, v28 op_sel:[0,0,1]
	v_cvt_pk_fp8_f32 v7, v27, v29 op_sel:[0,0,1]
	v_add_u32_e32 v10, s2, v21
	v_ashrrev_i32_e32 v31, 31, v30
	v_ashrrev_i32_e32 v11, 31, v10
	v_lshlrev_b64 v[30:31], 10, v[30:31]
	v_lshlrev_b64 v[10:11], 10, v[10:11]
	v_lshl_add_u64 v[30:31], v[4:5], 0, v[30:31]
	v_lshl_add_u64 v[4:5], v[4:5], 0, v[10:11]
	global_store_dwordx2 v[30:31], v[16:17], off
	global_store_dwordx2 v[4:5], v[6:7], off
	s_waitcnt lgkmcnt(0)
	s_branch .LBB0_1376

.LBB0_1876:
	v_lshlrev_b32_e32 v57, 16, v6
	v_and_b32_e32 v56, 0xffff0000, v8
	s_waitcnt vmcnt(3)
	v_lshlrev_b32_e32 v58, 16, v46
	v_and_b32_e32 v59, 0xffff0000, v46
	v_lshlrev_b32_e32 v60, 16, v47
	v_and_b32_e32 v61, 0xffff0000, v47
	v_lshlrev_b32_e32 v47, 16, v8
	v_and_b32_e32 v46, 0xffff0000, v6
	v_pk_mul_f32 v[56:57], v[2:3], v[56:57] op_sel:[1,0] op_sel_hi:[0,1]
	v_pk_fma_f32 v[46:47], v[2:3], v[46:47], v[56:57]
	v_lshlrev_b32_e32 v6, 16, v7
	v_pk_add_f32 v[42:43], v[42:43], v[46:47]
	v_and_b32_e32 v47, 0xffff0000, v7
	v_and_b32_e32 v7, 0xffff0000, v9
	v_lshlrev_b32_e32 v46, 16, v9
	v_pk_mul_f32 v[6:7], v[2:3], v[6:7]
	s_waitcnt vmcnt(2)
	v_lshlrev_b32_e32 v62, 16, v88
	v_pk_fma_f32 v[6:7], v[2:3], v[46:47], v[6:7] op_sel:[1,0,0] op_sel_hi:[0,1,1]
	v_pk_add_f32 v[8:9], v[40:41], v[6:7]
	v_mov_b32_e32 v6, v43
	v_mov_b32_e32 v7, v42
	global_store_dwordx4 v[22:23], v[6:9], off offset:-2048 nt
	v_and_b32_e32 v63, 0xffff0000, v88
	v_lshlrev_b32_e32 v64, 16, v89
	v_lshlrev_b32_e32 v8, 16, v10
	v_and_b32_e32 v9, 0xffff0000, v12
	v_lshlrev_b32_e32 v6, 16, v12
	v_and_b32_e32 v7, 0xffff0000, v10
	v_pk_mul_f32 v[8:9], v[2:3], v[8:9]
	v_lshlrev_b32_e32 v10, 16, v11
	v_pk_fma_f32 v[6:7], v[2:3], v[6:7], v[8:9] op_sel:[1,0,0] op_sel_hi:[0,1,1]
	v_and_b32_e32 v9, 0xffff0000, v11
	v_and_b32_e32 v11, 0xffff0000, v13
	v_lshlrev_b32_e32 v8, 16, v13
	v_pk_mul_f32 v[10:11], v[2:3], v[10:11]
	v_pk_add_f32 v[6:7], v[38:39], v[6:7]
	v_pk_fma_f32 v[8:9], v[2:3], v[8:9], v[10:11] op_sel:[1,0,0] op_sel_hi:[0,1,1]
	v_pk_add_f32 v[8:9], v[36:37], v[8:9]
	global_store_dwordx4 v[22:23], v[6:9], off offset:-1024 nt
	v_lshlrev_b32_e32 v10, 16, v15
	v_and_b32_e32 v11, 0xffff0000, v17
	v_lshlrev_b32_e32 v8, 16, v14
	v_and_b32_e32 v9, 0xffff0000, v16
	v_lshlrev_b32_e32 v6, 16, v16
	v_and_b32_e32 v7, 0xffff0000, v14
	v_pk_mul_f32 v[8:9], v[2:3], v[8:9]
	v_pk_mul_f32 v[10:11], v[2:3], v[10:11]
	v_pk_fma_f32 v[6:7], v[2:3], v[6:7], v[8:9] op_sel:[1,0,0] op_sel_hi:[0,1,1]
	v_lshlrev_b32_e32 v8, 16, v17
	v_and_b32_e32 v9, 0xffff0000, v15
	v_pk_fma_f32 v[8:9], v[2:3], v[8:9], v[10:11] op_sel:[1,0,0] op_sel_hi:[0,1,1]
	v_pk_add_f32 v[6:7], v[34:35], v[6:7]
	v_pk_add_f32 v[8:9], v[32:33], v[8:9]
	global_store_dwordx4 v[22:23], v[6:9], off nt
	v_lshlrev_b32_e32 v10, 16, v19
	v_and_b32_e32 v11, 0xffff0000, v21
	v_lshlrev_b32_e32 v8, 16, v18
	v_and_b32_e32 v9, 0xffff0000, v20
	v_lshlrev_b32_e32 v6, 16, v20
	v_and_b32_e32 v7, 0xffff0000, v18
	v_pk_mul_f32 v[8:9], v[2:3], v[8:9]
	v_pk_mul_f32 v[10:11], v[2:3], v[10:11]
	v_pk_fma_f32 v[6:7], v[2:3], v[6:7], v[8:9] op_sel:[1,0,0] op_sel_hi:[0,1,1]
	v_lshlrev_b32_e32 v8, 16, v21
	v_and_b32_e32 v9, 0xffff0000, v19
	v_pk_fma_f32 v[2:3], v[2:3], v[8:9], v[10:11] op_sel:[1,0,0] op_sel_hi:[0,1,1]
	v_and_b32_e32 v65, 0xffff0000, v89
	s_waitcnt vmcnt(4)
	v_lshlrev_b32_e32 v66, 16, v94
	v_and_b32_e32 v67, 0xffff0000, v94
	v_lshlrev_b32_e32 v68, 16, v95
	v_and_b32_e32 v69, 0xffff0000, v95
	s_waitcnt vmcnt(3)
	v_lshlrev_b32_e32 v70, 16, v98
	v_and_b32_e32 v71, 0xffff0000, v98
	v_lshlrev_b32_e32 v72, 16, v99
	v_and_b32_e32 v73, 0xffff0000, v99
	v_pk_add_f32 v[6:7], v[30:31], v[6:7]
	v_pk_add_f32 v[8:9], v[28:29], v[2:3]
	s_mov_b64 s[2:3], 0x800000
	global_store_dwordx4 v[22:23], v[6:9], off offset:1024 nt
	v_lshl_add_u64 v[22:23], v[22:23], 0, s[2:3]
	s_andn2_b64 vcc, exec, s[46:47]
	v_mov_b64_e32 v[2:3], v[0:1]
	v_mov_b64_e32 v[0:1], v[44:45]
	s_mov_b64 s[18:19], s[44:45]
	v_mov_b32_e32 v30, v70
	v_mov_b32_e32 v31, v71
	v_mov_b32_e32 v28, v72
	v_mov_b32_e32 v29, v73
	v_mov_b32_e32 v34, v66
	v_mov_b32_e32 v35, v67
	v_mov_b32_e32 v32, v68
	v_mov_b32_e32 v33, v69
	v_mov_b32_e32 v38, v62
	v_mov_b32_e32 v39, v63
	v_mov_b32_e32 v36, v64
	v_mov_b32_e32 v37, v65
	v_mov_b32_e32 v43, v58
	v_mov_b32_e32 v42, v59
	v_mov_b32_e32 v40, v60
	v_mov_b32_e32 v41, v61
	v_mov_b32_e32 v18, v52
	v_mov_b32_e32 v19, v53
	v_mov_b32_e32 v14, v92
	v_mov_b32_e32 v15, v93
	v_mov_b32_e32 v10, v78
	v_mov_b32_e32 v11, v79
	v_mov_b32_e32 v6, v48
	v_mov_b32_e32 v7, v49
	v_mov_b32_e32 v20, v50
	v_mov_b32_e32 v21, v51
	v_mov_b32_e32 v16, v96
	v_mov_b32_e32 v17, v97
	v_mov_b32_e32 v12, v90
	v_mov_b32_e32 v13, v91
	v_mov_b32_e32 v8, v54
	v_mov_b32_e32 v9, v55
	s_cbranch_vccnz .LBB0_1877
	s_getpc_b64 s[98:99]
